# 52 more provably non-blocking pre-barrier lgkmcnt waits deleted in the K-loop load segments (count >= reads outstanding)
# baseline (speedup 1.0000x reference)
.LBB0_220:
	s_add_u32 s40, s10, s38
	s_addc_u32 s41, s11, s39
	s_add_u32 s42, s40, 0x49800100
	ds_read_b128 v[144:147], v154
	ds_read_b128 v[170:173], v154 offset:2048
	ds_read_b128 v[148:151], v155
	ds_read_b128 v[174:177], v155 offset:2048
	s_addc_u32 s43, s41, 0
	s_add_u32 s67, s1, s38
	s_addc_u32 s68, s56, s39
	s_cmpk_eq_i32 s38, 0x700
	s_cselect_b64 vcc, -1, 0
	s_and_b64 s[40:41], vcc, exec
	ds_read_b128 v[178:181], v152
	ds_read_b128 v[186:189], v152 offset:2048
	ds_read_b128 v[182:185], v153
	ds_read_b128 v[190:193], v153 offset:2048
	ds_read_b128 v[196:199], v152 offset:4096
	ds_read_b128 v[204:207], v152 offset:6144
	ds_read_b128 v[200:203], v153 offset:4096
	ds_read_b128 v[208:211], v153 offset:6144
	s_waitcnt vmcnt(6)
	s_waitcnt lgkmcnt(8)
	s_barrier
	s_waitcnt lgkmcnt(0)
	s_setprio 1
	v_mfma_f32_16x16x128_f8f6f4 v[124:127], v[144:151], v[178:185], v[124:127]
	v_mfma_f32_16x16x128_f8f6f4 v[120:123], v[170:177], v[178:185], v[120:123]
	v_mfma_f32_16x16x128_f8f6f4 v[108:111], v[144:151], v[186:193], v[108:111]
	v_mfma_f32_16x16x128_f8f6f4 v[104:107], v[170:177], v[186:193], v[104:107]
	v_mfma_f32_16x16x128_f8f6f4 v[92:95], v[144:151], v[196:203], v[92:95]
	v_mfma_f32_16x16x128_f8f6f4 v[88:91], v[170:177], v[196:203], v[88:91]
	v_mfma_f32_16x16x128_f8f6f4 v[76:79], v[144:151], v[204:211], v[76:79]
	v_mfma_f32_16x16x128_f8f6f4 v[72:75], v[170:177], v[204:211], v[72:75]
	s_setprio 0
	s_barrier
	ds_read_b128 v[222:225], v154 offset:16384
	ds_read_b128 v[230:233], v154 offset:18432
	ds_read_b128 v[226:229], v155 offset:16384
	ds_read_b128 v[234:237], v155 offset:18432
	v_cndmask_b32_e32 v132, v135, v165, vcc
	s_cselect_b32 s43, s13, s43
	s_cselect_b32 s42, s12, s42
	s_cselect_b32 s41, s37, s68
	s_cselect_b32 s40, s36, s67
	v_cndmask_b32_e32 v137, v136, v167, vcc
	v_lshl_add_u64 v[212:213], v[142:143], 0, s[38:39]
	s_add_i32 m0, s33, 0xc000
	s_nop 0
	global_load_lds_dwordx4 v[212:213], off
	v_lshl_add_u64 v[212:213], v[140:141], 0, s[38:39]
	s_add_i32 m0, s33, 0xe000
	v_cndmask_b32_e32 v220, v134, v166, vcc
	global_load_lds_dwordx4 v[212:213], off
	s_barrier
	s_waitcnt lgkmcnt(0)
	s_setprio 1
	v_mfma_f32_16x16x128_f8f6f4 v[116:119], v[222:229], v[178:185], v[116:119]
	v_mfma_f32_16x16x128_f8f6f4 v[112:115], v[230:237], v[178:185], v[112:115]
	v_mfma_f32_16x16x128_f8f6f4 v[100:103], v[222:229], v[186:193], v[100:103]
	v_mfma_f32_16x16x128_f8f6f4 v[96:99], v[230:237], v[186:193], v[96:99]
	v_mfma_f32_16x16x128_f8f6f4 v[84:87], v[222:229], v[196:203], v[84:87]
	v_mfma_f32_16x16x128_f8f6f4 v[80:83], v[230:237], v[196:203], v[80:83]
	v_mfma_f32_16x16x128_f8f6f4 v[68:71], v[222:229], v[204:211], v[68:71]
	v_mfma_f32_16x16x128_f8f6f4 v[64:67], v[230:237], v[204:211], v[64:67]
	s_setprio 0
	s_barrier
	s_mov_b32 m0, s33
	ds_read_b128 v[186:189], v152 offset:16384
	ds_read_b128 v[196:199], v152 offset:18432
	ds_read_b128 v[190:193], v153 offset:16384
	ds_read_b128 v[200:203], v153 offset:18432
	ds_read_b128 v[204:207], v152 offset:20480
	ds_read_b128 v[212:215], v152 offset:22528
	ds_read_b128 v[208:211], v153 offset:20480
	ds_read_b128 v[216:219], v153 offset:22528
	global_load_lds_dwordx4 v132, s[42:43]
	s_mov_b32 m0, s46
	v_mov_b32_e32 v221, v133
	global_load_lds_dwordx4 v220, s[42:43]
	s_barrier
	s_waitcnt lgkmcnt(0)
	v_lshl_add_u64 v[246:247], s[42:43], 0, v[132:133]
	v_lshl_add_u64 v[244:245], s[42:43], 0, v[220:221]
	s_setprio 1
	s_waitcnt lgkmcnt(0)
	v_mfma_f32_16x16x128_f8f6f4 v[60:63], v[144:151], v[186:193], v[60:63]
	v_mfma_f32_16x16x128_f8f6f4 v[56:59], v[170:177], v[186:193], v[56:59]
	v_mfma_f32_16x16x128_f8f6f4 v[44:47], v[144:151], v[196:203], v[44:47]
	v_mfma_f32_16x16x128_f8f6f4 v[40:43], v[170:177], v[196:203], v[40:43]
	v_mfma_f32_16x16x128_f8f6f4 v[28:31], v[144:151], v[204:211], v[28:31]
	v_mfma_f32_16x16x128_f8f6f4 v[24:27], v[170:177], v[204:211], v[24:27]
	v_mfma_f32_16x16x128_f8f6f4 v[12:15], v[144:151], v[212:219], v[12:15]
	v_mfma_f32_16x16x128_f8f6f4 v[8:11], v[170:177], v[212:219], v[8:11]
	s_setprio 0
	s_barrier
	s_mov_b32 m0, s44
	v_lshl_add_u64 v[144:145], s[40:41], 0, v[128:129]
	global_load_lds_dwordx4 v[144:145], off
	v_lshl_add_u64 v[146:147], s[40:41], 0, v[130:131]
	s_mov_b32 m0, s45
	s_nop 0
	global_load_lds_dwordx4 v[146:147], off
	s_waitcnt vmcnt(8)
	s_barrier
	s_setprio 1
	s_waitcnt lgkmcnt(0)
	v_mfma_f32_16x16x128_f8f6f4 v[52:55], v[222:229], v[186:193], v[52:55]
	v_mfma_f32_16x16x128_f8f6f4 v[48:51], v[230:237], v[186:193], v[48:51]
	v_mfma_f32_16x16x128_f8f6f4 v[36:39], v[222:229], v[196:203], v[36:39]
	v_mfma_f32_16x16x128_f8f6f4 v[32:35], v[230:237], v[196:203], v[32:35]
	v_mfma_f32_16x16x128_f8f6f4 v[20:23], v[222:229], v[204:211], v[20:23]
	v_mfma_f32_16x16x128_f8f6f4 v[16:19], v[230:237], v[204:211], v[16:19]
	v_mfma_f32_16x16x128_f8f6f4 v[4:7], v[222:229], v[212:219], v[4:7]
	v_mfma_f32_16x16x128_f8f6f4 v[0:3], v[230:237], v[212:219], v[0:3]
	s_setprio 0
	s_barrier
	ds_read_b128 v[170:173], v154 offset:32768
	ds_read_b128 v[178:181], v154 offset:34816
	ds_read_b128 v[174:177], v155 offset:32768
	ds_read_b128 v[182:185], v155 offset:34816
	s_mov_b32 m0, s49
	ds_read_b128 v[186:189], v152 offset:32768
	ds_read_b128 v[196:199], v152 offset:34816
	ds_read_b128 v[190:193], v153 offset:32768
	ds_read_b128 v[200:203], v153 offset:34816
	ds_read_b128 v[204:207], v152 offset:36864
	ds_read_b128 v[212:215], v152 offset:38912
	ds_read_b128 v[208:211], v153 offset:36864
	ds_read_b128 v[216:219], v153 offset:38912
	v_cndmask_b32_e32 v132, v138, v168, vcc
	global_load_lds_dwordx4 v137, s[42:43]
	s_mov_b32 m0, s50
	s_nop 0
	global_load_lds_dwordx4 v132, s[42:43]
	s_waitcnt vmcnt(8)
	s_waitcnt lgkmcnt(8)
	s_barrier
	s_waitcnt lgkmcnt(0)
	s_setprio 1
	v_mfma_f32_16x16x128_f8f6f4 v[124:127], v[170:177], v[186:193], v[124:127]
	v_mfma_f32_16x16x128_f8f6f4 v[120:123], v[178:185], v[186:193], v[120:123]
	v_mfma_f32_16x16x128_f8f6f4 v[108:111], v[170:177], v[196:203], v[108:111]
	v_mfma_f32_16x16x128_f8f6f4 v[104:107], v[178:185], v[196:203], v[104:107]
	v_mfma_f32_16x16x128_f8f6f4 v[92:95], v[170:177], v[204:211], v[92:95]
	v_mfma_f32_16x16x128_f8f6f4 v[88:91], v[178:185], v[204:211], v[88:91]
	v_mfma_f32_16x16x128_f8f6f4 v[76:79], v[170:177], v[212:219], v[76:79]
	v_mfma_f32_16x16x128_f8f6f4 v[72:75], v[178:185], v[212:219], v[72:75]
	s_setprio 0
	s_barrier
	ds_read_b128 v[222:225], v154 offset:49152
	ds_read_b128 v[230:233], v154 offset:51200
	ds_read_b128 v[226:229], v155 offset:49152
	ds_read_b128 v[234:237], v155 offset:51200
	s_add_u32 s42, s40, 0x4000
	s_addc_u32 s43, s41, 0
	v_lshl_add_u64 v[220:221], s[42:43], 0, v[128:129]
	s_mov_b32 m0, s47
	s_nop 0
	global_load_lds_dwordx4 v[220:221], off
	v_lshl_add_u64 v[220:221], s[42:43], 0, v[130:131]
	s_mov_b32 m0, s48
	s_nop 0
	global_load_lds_dwordx4 v[220:221], off
	s_waitcnt vmcnt(8)
	s_barrier
	s_waitcnt lgkmcnt(0)
	s_setprio 1
	v_mfma_f32_16x16x128_f8f6f4 v[116:119], v[222:229], v[186:193], v[116:119]
	v_mfma_f32_16x16x128_f8f6f4 v[112:115], v[230:237], v[186:193], v[112:115]
	v_mfma_f32_16x16x128_f8f6f4 v[100:103], v[222:229], v[196:203], v[100:103]
	v_mfma_f32_16x16x128_f8f6f4 v[96:99], v[230:237], v[196:203], v[96:99]
	v_mfma_f32_16x16x128_f8f6f4 v[84:87], v[222:229], v[204:211], v[84:87]
	v_mfma_f32_16x16x128_f8f6f4 v[80:83], v[230:237], v[204:211], v[80:83]
	v_mfma_f32_16x16x128_f8f6f4 v[68:71], v[222:229], v[212:219], v[68:71]
	v_mfma_f32_16x16x128_f8f6f4 v[64:67], v[230:237], v[212:219], v[64:67]
	s_setprio 0
	s_barrier
	s_mov_b32 m0, s54
	v_lshl_add_u64 v[246:247], v[246:247], 0, s[24:25]
	ds_read_b128 v[186:189], v152 offset:49152
	ds_read_b128 v[196:199], v152 offset:51200
	ds_read_b128 v[190:193], v153 offset:49152
	ds_read_b128 v[200:203], v153 offset:51200
	ds_read_b128 v[204:207], v152 offset:53248
	ds_read_b128 v[212:215], v152 offset:55296
	ds_read_b128 v[208:211], v153 offset:53248
	ds_read_b128 v[216:219], v153 offset:55296
	global_load_lds_dwordx4 v[246:247], off
	v_lshl_add_u64 v[244:245], v[244:245], 0, s[24:25]
	s_mov_b32 m0, s55
	s_nop 0
	global_load_lds_dwordx4 v[244:245], off
	s_barrier
	s_waitcnt lgkmcnt(0)
	s_setprio 1
	v_mfma_f32_16x16x128_f8f6f4 v[60:63], v[170:177], v[186:193], v[60:63]
	v_mfma_f32_16x16x128_f8f6f4 v[56:59], v[178:185], v[186:193], v[56:59]
	v_mfma_f32_16x16x128_f8f6f4 v[44:47], v[170:177], v[196:203], v[44:47]
	v_mfma_f32_16x16x128_f8f6f4 v[40:43], v[178:185], v[196:203], v[40:43]
	v_mfma_f32_16x16x128_f8f6f4 v[28:31], v[170:177], v[204:211], v[28:31]
	v_mfma_f32_16x16x128_f8f6f4 v[24:27], v[178:185], v[204:211], v[24:27]
	v_mfma_f32_16x16x128_f8f6f4 v[12:15], v[170:177], v[212:219], v[12:15]
	v_mfma_f32_16x16x128_f8f6f4 v[8:11], v[178:185], v[212:219], v[8:11]
	s_setprio 0
	s_barrier
	s_mov_b32 m0, s52
	v_lshl_add_u64 v[144:145], v[144:145], 0, s[24:25]
	global_load_lds_dwordx4 v[144:145], off
	v_lshl_add_u64 v[144:145], v[146:147], 0, s[24:25]
	s_mov_b32 m0, s53
	s_nop 0
	global_load_lds_dwordx4 v[144:145], off
	s_waitcnt vmcnt(8)
	s_barrier
	s_setprio 1
	s_waitcnt lgkmcnt(0)
	v_mfma_f32_16x16x128_f8f6f4 v[52:55], v[222:229], v[186:193], v[52:55]
	v_mfma_f32_16x16x128_f8f6f4 v[48:51], v[230:237], v[186:193], v[48:51]
	v_mfma_f32_16x16x128_f8f6f4 v[36:39], v[222:229], v[196:203], v[36:39]
	v_mfma_f32_16x16x128_f8f6f4 v[32:35], v[230:237], v[196:203], v[32:35]
	v_mfma_f32_16x16x128_f8f6f4 v[20:23], v[222:229], v[204:211], v[20:23]
	v_mfma_f32_16x16x128_f8f6f4 v[16:19], v[230:237], v[204:211], v[16:19]
	v_mfma_f32_16x16x128_f8f6f4 v[4:7], v[222:229], v[212:219], v[4:7]
	v_mfma_f32_16x16x128_f8f6f4 v[0:3], v[230:237], v[212:219], v[0:3]
	s_setprio 0
	s_barrier
	s_add_u32 s40, s40, 0x4080
	s_addc_u32 s41, s41, 0
	s_mov_b32 m0, s58
	v_lshl_add_u64 v[144:145], s[40:41], 0, v[128:129]
	global_load_lds_dwordx4 v[144:145], off
	v_lshl_add_u64 v[144:145], s[40:41], 0, v[130:131]
	s_mov_b32 m0, s59
	s_add_i32 s57, s57, 2
	global_load_lds_dwordx4 v[144:145], off
	s_add_u32 s38, s38, 0x100
	s_addc_u32 s39, s39, 0
	s_cmp_gt_u32 s57, 13
	s_cbranch_scc0 .LBB0_220
	s_and_b64 vcc, exec, s[28:29]
	s_cbranch_vccz .LBB0_223
	s_barrier

.LBB0_313:
	s_add_u32 s36, s6, s34
	s_addc_u32 s37, s7, s35
	s_add_u32 s38, s36, 0x4e000100
	ds_read_b128 v[158:161], v167
	ds_read_b128 v[172:175], v167 offset:2048
	ds_read_b128 v[162:165], v168
	ds_read_b128 v[176:179], v168 offset:2048
	s_addc_u32 s39, s37, 0
	s_add_u32 s70, s67, s34
	s_addc_u32 s71, s68, s35
	s_cmpk_eq_i32 s34, 0x200
	s_cselect_b64 vcc, -1, 0
	s_and_b64 s[36:37], vcc, exec
	ds_read_b128 v[180:183], v129
	ds_read_b128 v[196:199], v129 offset:2048
	ds_read_b128 v[184:187], v131
	ds_read_b128 v[200:203], v131 offset:2048
	ds_read_b128 v[204:207], v129 offset:4096
	ds_read_b128 v[212:215], v129 offset:6144
	ds_read_b128 v[208:211], v131 offset:4096
	ds_read_b128 v[216:219], v131 offset:6144
	s_waitcnt vmcnt(6)
	s_waitcnt lgkmcnt(8)
	s_barrier
	s_waitcnt lgkmcnt(0)
	v_cndmask_b32_e32 v188, v148, v140, vcc
	s_setprio 1
	s_waitcnt lgkmcnt(0)
	v_mfma_f32_16x16x128_f8f6f4 v[124:127], v[158:165], v[180:187], v[124:127]
	v_mfma_f32_16x16x128_f8f6f4 v[120:123], v[172:179], v[180:187], v[120:123]
	v_mfma_f32_16x16x128_f8f6f4 v[112:115], v[158:165], v[196:203], v[112:115]
	v_mfma_f32_16x16x128_f8f6f4 v[104:107], v[172:179], v[196:203], v[104:107]
	v_mfma_f32_16x16x128_f8f6f4 v[96:99], v[158:165], v[204:211], v[96:99]
	v_mfma_f32_16x16x128_f8f6f4 v[88:91], v[172:179], v[204:211], v[88:91]
	v_mfma_f32_16x16x128_f8f6f4 v[80:83], v[158:165], v[212:219], v[80:83]
	v_mfma_f32_16x16x128_f8f6f4 v[72:75], v[172:179], v[212:219], v[72:75]
	s_setprio 0
	s_barrier
	ds_read_b128 v[228:231], v167 offset:16384
	ds_read_b128 v[236:239], v167 offset:18432
	ds_read_b128 v[232:235], v168 offset:16384
	ds_read_b128 v[240:243], v168 offset:18432
	v_cndmask_b32_e32 v136, v146, v138, vcc
	s_cselect_b32 s39, s9, s39
	s_cselect_b32 s38, s8, s38
	s_cselect_b32 s37, s31, s71
	s_cselect_b32 s36, s30, s70
	v_cndmask_b32_e32 v139, v150, v142, vcc
	v_lshl_add_u64 v[252:253], v[156:157], 0, s[34:35]
	s_add_i32 m0, s46, 0xc000
	s_nop 0
	global_load_lds_dwordx4 v[252:253], off
	v_lshl_add_u64 v[252:253], v[154:155], 0, s[34:35]
	s_add_i32 m0, s46, 0xe000
	s_nop 0
	global_load_lds_dwordx4 v[252:253], off
	s_barrier
	s_waitcnt lgkmcnt(0)
	s_setprio 1
	v_mfma_f32_16x16x128_f8f6f4 v[116:119], v[228:235], v[180:187], v[116:119]
	v_mfma_f32_16x16x128_f8f6f4 v[108:111], v[236:243], v[180:187], v[108:111]
	v_mfma_f32_16x16x128_f8f6f4 v[100:103], v[228:235], v[196:203], v[100:103]
	v_mfma_f32_16x16x128_f8f6f4 v[92:95], v[236:243], v[196:203], v[92:95]
	v_mfma_f32_16x16x128_f8f6f4 v[84:87], v[228:235], v[204:211], v[84:87]
	v_mfma_f32_16x16x128_f8f6f4 v[76:79], v[236:243], v[204:211], v[76:79]
	v_mfma_f32_16x16x128_f8f6f4 v[68:71], v[228:235], v[212:219], v[68:71]
	v_mfma_f32_16x16x128_f8f6f4 v[64:67], v[236:243], v[212:219], v[64:67]
	s_setprio 0
	s_barrier
	s_mov_b32 m0, s46
	ds_read_b128 v[196:199], v129 offset:16384
	ds_read_b128 v[204:207], v129 offset:18432
	ds_read_b128 v[200:203], v131 offset:16384
	ds_read_b128 v[208:211], v131 offset:18432
	ds_read_b128 v[212:215], v129 offset:20480
	ds_read_b128 v[220:223], v129 offset:22528
	ds_read_b128 v[216:219], v131 offset:20480
	ds_read_b128 v[224:227], v131 offset:22528
	global_load_lds_dwordx4 v136, s[38:39]
	s_mov_b32 m0, s49
	v_mov_b32_e32 v189, v137
	global_load_lds_dwordx4 v188, s[38:39]
	s_barrier
	s_waitcnt lgkmcnt(0)
	v_lshl_add_u64 v[246:247], s[38:39], 0, v[136:137]
	v_lshl_add_u64 v[244:245], s[38:39], 0, v[188:189]
	s_setprio 1
	s_waitcnt lgkmcnt(0)
	v_mfma_f32_16x16x128_f8f6f4 v[60:63], v[158:165], v[196:203], v[60:63]
	v_mfma_f32_16x16x128_f8f6f4 v[56:59], v[172:179], v[196:203], v[56:59]
	v_mfma_f32_16x16x128_f8f6f4 v[48:51], v[158:165], v[204:211], v[48:51]
	v_mfma_f32_16x16x128_f8f6f4 v[40:43], v[172:179], v[204:211], v[40:43]
	v_mfma_f32_16x16x128_f8f6f4 v[32:35], v[158:165], v[212:219], v[32:35]
	v_mfma_f32_16x16x128_f8f6f4 v[24:27], v[172:179], v[212:219], v[24:27]
	v_mfma_f32_16x16x128_f8f6f4 v[16:19], v[158:165], v[220:227], v[16:19]
	v_mfma_f32_16x16x128_f8f6f4 v[8:11], v[172:179], v[220:227], v[8:11]
	s_setprio 0
	s_barrier
	s_mov_b32 m0, s47
	v_lshl_add_u64 v[158:159], s[36:37], 0, v[134:135]
	global_load_lds_dwordx4 v[158:159], off
	v_lshl_add_u64 v[160:161], s[36:37], 0, v[132:133]
	s_mov_b32 m0, s48
	s_nop 0
	global_load_lds_dwordx4 v[160:161], off
	s_waitcnt vmcnt(8)
	s_barrier
	s_setprio 1
	s_waitcnt lgkmcnt(0)
	v_mfma_f32_16x16x128_f8f6f4 v[52:55], v[228:235], v[196:203], v[52:55]
	v_mfma_f32_16x16x128_f8f6f4 v[44:47], v[236:243], v[196:203], v[44:47]
	v_mfma_f32_16x16x128_f8f6f4 v[36:39], v[228:235], v[204:211], v[36:39]
	v_mfma_f32_16x16x128_f8f6f4 v[28:31], v[236:243], v[204:211], v[28:31]
	v_mfma_f32_16x16x128_f8f6f4 v[20:23], v[228:235], v[212:219], v[20:23]
	v_mfma_f32_16x16x128_f8f6f4 v[12:15], v[236:243], v[212:219], v[12:15]
	v_mfma_f32_16x16x128_f8f6f4 v[4:7], v[228:235], v[220:227], v[4:7]
	v_mfma_f32_16x16x128_f8f6f4 v[0:3], v[236:243], v[220:227], v[0:3]
	s_setprio 0
	s_barrier
	ds_read_b128 v[172:175], v167 offset:32768
	ds_read_b128 v[180:183], v167 offset:34816
	ds_read_b128 v[176:179], v168 offset:32768
	ds_read_b128 v[184:187], v168 offset:34816
	s_mov_b32 m0, s52
	ds_read_b128 v[196:199], v129 offset:32768
	ds_read_b128 v[204:207], v129 offset:34816
	ds_read_b128 v[200:203], v131 offset:32768
	ds_read_b128 v[208:211], v131 offset:34816
	ds_read_b128 v[212:215], v129 offset:36864
	ds_read_b128 v[220:223], v129 offset:38912
	ds_read_b128 v[216:219], v131 offset:36864
	ds_read_b128 v[224:227], v131 offset:38912
	v_cndmask_b32_e32 v136, v152, v144, vcc
	global_load_lds_dwordx4 v139, s[38:39]
	s_mov_b32 m0, s53
	s_nop 0
	global_load_lds_dwordx4 v136, s[38:39]
	s_waitcnt vmcnt(8)
	s_waitcnt lgkmcnt(8)
	s_barrier
	s_waitcnt lgkmcnt(0)
	s_setprio 1
	v_mfma_f32_16x16x128_f8f6f4 v[124:127], v[172:179], v[196:203], v[124:127]
	v_mfma_f32_16x16x128_f8f6f4 v[120:123], v[180:187], v[196:203], v[120:123]
	v_mfma_f32_16x16x128_f8f6f4 v[112:115], v[172:179], v[204:211], v[112:115]
	v_mfma_f32_16x16x128_f8f6f4 v[104:107], v[180:187], v[204:211], v[104:107]
	v_mfma_f32_16x16x128_f8f6f4 v[96:99], v[172:179], v[212:219], v[96:99]
	v_mfma_f32_16x16x128_f8f6f4 v[88:91], v[180:187], v[212:219], v[88:91]
	v_mfma_f32_16x16x128_f8f6f4 v[80:83], v[172:179], v[220:227], v[80:83]
	v_mfma_f32_16x16x128_f8f6f4 v[72:75], v[180:187], v[220:227], v[72:75]
	s_setprio 0
	s_barrier
	ds_read_b128 v[228:231], v167 offset:49152
	ds_read_b128 v[236:239], v167 offset:51200
	ds_read_b128 v[232:235], v168 offset:49152
	ds_read_b128 v[240:243], v168 offset:51200
	s_add_u32 s38, s36, 0x1800
	s_addc_u32 s39, s37, 0
	v_lshl_add_u64 v[188:189], s[38:39], 0, v[134:135]
	s_mov_b32 m0, s50
	s_nop 0
	global_load_lds_dwordx4 v[188:189], off
	v_lshl_add_u64 v[188:189], s[38:39], 0, v[132:133]
	s_mov_b32 m0, s51
	s_nop 0
	global_load_lds_dwordx4 v[188:189], off
	s_waitcnt vmcnt(8)
	s_barrier
	s_waitcnt lgkmcnt(0)
	s_setprio 1
	v_mfma_f32_16x16x128_f8f6f4 v[116:119], v[228:235], v[196:203], v[116:119]
	v_mfma_f32_16x16x128_f8f6f4 v[108:111], v[236:243], v[196:203], v[108:111]
	v_mfma_f32_16x16x128_f8f6f4 v[100:103], v[228:235], v[204:211], v[100:103]
	v_mfma_f32_16x16x128_f8f6f4 v[92:95], v[236:243], v[204:211], v[92:95]
	v_mfma_f32_16x16x128_f8f6f4 v[84:87], v[228:235], v[212:219], v[84:87]
	v_mfma_f32_16x16x128_f8f6f4 v[76:79], v[236:243], v[212:219], v[76:79]
	v_mfma_f32_16x16x128_f8f6f4 v[68:71], v[228:235], v[220:227], v[68:71]
	v_mfma_f32_16x16x128_f8f6f4 v[64:67], v[236:243], v[220:227], v[64:67]
	s_setprio 0
	s_barrier
	s_mov_b32 m0, s56
	v_lshl_add_u64 v[246:247], v[246:247], 0, s[18:19]
	ds_read_b128 v[196:199], v129 offset:49152
	ds_read_b128 v[204:207], v129 offset:51200
	ds_read_b128 v[200:203], v131 offset:49152
	ds_read_b128 v[208:211], v131 offset:51200
	ds_read_b128 v[212:215], v129 offset:53248
	ds_read_b128 v[220:223], v129 offset:55296
	ds_read_b128 v[216:219], v131 offset:53248
	ds_read_b128 v[224:227], v131 offset:55296
	global_load_lds_dwordx4 v[246:247], off
	v_lshl_add_u64 v[244:245], v[244:245], 0, s[18:19]
	s_mov_b32 m0, s57
	s_nop 0
	global_load_lds_dwordx4 v[244:245], off
	s_barrier
	s_waitcnt lgkmcnt(0)
	s_setprio 1
	v_mfma_f32_16x16x128_f8f6f4 v[60:63], v[172:179], v[196:203], v[60:63]
	v_mfma_f32_16x16x128_f8f6f4 v[56:59], v[180:187], v[196:203], v[56:59]
	v_mfma_f32_16x16x128_f8f6f4 v[48:51], v[172:179], v[204:211], v[48:51]
	v_mfma_f32_16x16x128_f8f6f4 v[40:43], v[180:187], v[204:211], v[40:43]
	v_mfma_f32_16x16x128_f8f6f4 v[32:35], v[172:179], v[212:219], v[32:35]
	v_mfma_f32_16x16x128_f8f6f4 v[24:27], v[180:187], v[212:219], v[24:27]
	v_mfma_f32_16x16x128_f8f6f4 v[16:19], v[172:179], v[220:227], v[16:19]
	v_mfma_f32_16x16x128_f8f6f4 v[8:11], v[180:187], v[220:227], v[8:11]
	s_setprio 0
	s_barrier
	s_mov_b32 m0, s54
	v_lshl_add_u64 v[158:159], v[158:159], 0, s[18:19]
	global_load_lds_dwordx4 v[158:159], off
	v_lshl_add_u64 v[158:159], v[160:161], 0, s[18:19]
	s_mov_b32 m0, s55
	s_nop 0
	global_load_lds_dwordx4 v[158:159], off
	s_waitcnt vmcnt(8)
	s_barrier
	s_setprio 1
	s_waitcnt lgkmcnt(0)
	v_mfma_f32_16x16x128_f8f6f4 v[52:55], v[228:235], v[196:203], v[52:55]
	v_mfma_f32_16x16x128_f8f6f4 v[44:47], v[236:243], v[196:203], v[44:47]
	v_mfma_f32_16x16x128_f8f6f4 v[36:39], v[228:235], v[204:211], v[36:39]
	v_mfma_f32_16x16x128_f8f6f4 v[28:31], v[236:243], v[204:211], v[28:31]
	v_mfma_f32_16x16x128_f8f6f4 v[20:23], v[228:235], v[212:219], v[20:23]
	v_mfma_f32_16x16x128_f8f6f4 v[12:15], v[236:243], v[212:219], v[12:15]
	v_mfma_f32_16x16x128_f8f6f4 v[4:7], v[228:235], v[220:227], v[4:7]
	v_mfma_f32_16x16x128_f8f6f4 v[0:3], v[236:243], v[220:227], v[0:3]
	s_setprio 0
	s_barrier
	s_add_u32 s36, s36, 0x1880
	s_addc_u32 s37, s37, 0
	s_mov_b32 m0, s58
	v_lshl_add_u64 v[158:159], s[36:37], 0, v[134:135]
	global_load_lds_dwordx4 v[158:159], off
	v_lshl_add_u64 v[158:159], s[36:37], 0, v[132:133]
	s_mov_b32 m0, s59
	s_add_i32 s69, s69, 2
	global_load_lds_dwordx4 v[158:159], off
	s_add_u32 s34, s34, 0x100
	s_addc_u32 s35, s35, 0
	s_cmp_gt_u32 s69, 3
	s_cbranch_scc0 .LBB0_313
	s_and_b64 vcc, exec, s[24:25]
	s_cbranch_vccz .LBB0_316
	s_barrier

.LBB0_756:
	s_add_u32 s38, s8, s36
	s_addc_u32 s39, s9, s37
	s_add_u32 s40, s38, 0x14000100
	ds_read_b128 v[144:147], v154
	ds_read_b128 v[168:171], v154 offset:2048
	ds_read_b128 v[148:151], v155
	ds_read_b128 v[172:175], v155 offset:2048
	s_addc_u32 s41, s39, 0
	s_add_u32 s68, s0, s36
	s_addc_u32 s69, s1, s37
	s_cmpk_eq_i32 s36, 0x700
	s_cselect_b64 vcc, -1, 0
	s_and_b64 s[38:39], vcc, exec
	ds_read_b128 v[176:179], v152
	ds_read_b128 v[184:187], v152 offset:2048
	ds_read_b128 v[180:183], v153
	ds_read_b128 v[188:191], v153 offset:2048
	ds_read_b128 v[196:199], v152 offset:4096
	ds_read_b128 v[204:207], v152 offset:6144
	ds_read_b128 v[200:203], v153 offset:4096
	ds_read_b128 v[208:211], v153 offset:6144
	s_waitcnt vmcnt(6)
	s_waitcnt lgkmcnt(8)
	s_barrier
	s_waitcnt lgkmcnt(0)
	v_cndmask_b32_e32 v192, v134, v163, vcc
	s_setprio 1
	s_waitcnt lgkmcnt(0)
	v_mfma_f32_16x16x128_f8f6f4 v[124:127], v[144:151], v[176:183], v[124:127]
	v_mfma_f32_16x16x128_f8f6f4 v[120:123], v[168:175], v[176:183], v[120:123]
	v_mfma_f32_16x16x128_f8f6f4 v[108:111], v[144:151], v[184:191], v[108:111]
	v_mfma_f32_16x16x128_f8f6f4 v[104:107], v[168:175], v[184:191], v[104:107]
	v_mfma_f32_16x16x128_f8f6f4 v[92:95], v[144:151], v[196:203], v[92:95]
	v_mfma_f32_16x16x128_f8f6f4 v[88:91], v[168:175], v[196:203], v[88:91]
	v_mfma_f32_16x16x128_f8f6f4 v[76:79], v[144:151], v[204:211], v[76:79]
	v_mfma_f32_16x16x128_f8f6f4 v[72:75], v[168:175], v[204:211], v[72:75]
	s_setprio 0
	s_barrier
	ds_read_b128 v[234:237], v154 offset:16384
	ds_read_b128 v[242:245], v154 offset:18432
	ds_read_b128 v[238:241], v155 offset:16384
	ds_read_b128 v[246:249], v155 offset:18432
	v_cndmask_b32_e32 v132, v166, v162, vcc
	s_cselect_b32 s41, s11, s41
	s_cselect_b32 s40, s10, s40
	s_cselect_b32 s39, s31, s69
	s_cselect_b32 s38, s30, s68
	v_cndmask_b32_e32 v137, v136, v164, vcc
	s_mov_b32 m0, s66
	v_lshl_add_u64 v[220:221], v[142:143], 0, s[36:37]
	global_load_lds_dwordx4 v[220:221], off
	v_lshl_add_u64 v[220:221], v[140:141], 0, s[36:37]
	s_mov_b32 m0, s67
	s_nop 0
	global_load_lds_dwordx4 v[220:221], off
	s_barrier
	s_waitcnt lgkmcnt(0)
	s_setprio 1
	v_mfma_f32_16x16x128_f8f6f4 v[116:119], v[234:241], v[176:183], v[116:119]
	v_mfma_f32_16x16x128_f8f6f4 v[112:115], v[242:249], v[176:183], v[112:115]
	v_mfma_f32_16x16x128_f8f6f4 v[100:103], v[234:241], v[184:191], v[100:103]
	v_mfma_f32_16x16x128_f8f6f4 v[96:99], v[242:249], v[184:191], v[96:99]
	v_mfma_f32_16x16x128_f8f6f4 v[84:87], v[234:241], v[196:203], v[84:87]
	v_mfma_f32_16x16x128_f8f6f4 v[80:83], v[242:249], v[196:203], v[80:83]
	v_mfma_f32_16x16x128_f8f6f4 v[68:71], v[234:241], v[204:211], v[68:71]
	v_mfma_f32_16x16x128_f8f6f4 v[64:67], v[242:249], v[204:211], v[64:67]
	s_setprio 0
	s_barrier
	s_mov_b32 m0, s35
	ds_read_b128 v[184:187], v152 offset:16384
	ds_read_b128 v[196:199], v152 offset:18432
	ds_read_b128 v[188:191], v153 offset:16384
	ds_read_b128 v[200:203], v153 offset:18432
	ds_read_b128 v[204:207], v152 offset:20480
	ds_read_b128 v[212:215], v152 offset:22528
	ds_read_b128 v[208:211], v153 offset:20480
	ds_read_b128 v[216:219], v153 offset:22528
	global_load_lds_dwordx4 v132, s[40:41]
	s_mov_b32 m0, s45
	v_mov_b32_e32 v193, v133
	global_load_lds_dwordx4 v192, s[40:41]
	s_barrier
	s_waitcnt lgkmcnt(0)
	v_lshl_add_u64 v[252:253], s[40:41], 0, v[132:133]
	v_lshl_add_u64 v[250:251], s[40:41], 0, v[192:193]
	s_setprio 1
	s_waitcnt lgkmcnt(0)
	v_mfma_f32_16x16x128_f8f6f4 v[60:63], v[144:151], v[184:191], v[60:63]
	v_mfma_f32_16x16x128_f8f6f4 v[56:59], v[168:175], v[184:191], v[56:59]
	v_mfma_f32_16x16x128_f8f6f4 v[44:47], v[144:151], v[196:203], v[44:47]
	v_mfma_f32_16x16x128_f8f6f4 v[40:43], v[168:175], v[196:203], v[40:43]
	v_mfma_f32_16x16x128_f8f6f4 v[28:31], v[144:151], v[204:211], v[28:31]
	v_mfma_f32_16x16x128_f8f6f4 v[24:27], v[168:175], v[204:211], v[24:27]
	v_mfma_f32_16x16x128_f8f6f4 v[12:15], v[144:151], v[212:219], v[12:15]
	v_mfma_f32_16x16x128_f8f6f4 v[8:11], v[168:175], v[212:219], v[8:11]
	s_setprio 0
	s_barrier
	s_mov_b32 m0, s43
	v_lshl_add_u64 v[144:145], s[38:39], 0, v[130:131]
	global_load_lds_dwordx4 v[144:145], off
	v_lshl_add_u64 v[146:147], s[38:39], 0, v[128:129]
	s_mov_b32 m0, s44
	s_nop 0
	global_load_lds_dwordx4 v[146:147], off
	s_waitcnt vmcnt(8)
	s_barrier
	s_setprio 1
	s_waitcnt lgkmcnt(0)
	v_mfma_f32_16x16x128_f8f6f4 v[52:55], v[234:241], v[184:191], v[52:55]
	v_mfma_f32_16x16x128_f8f6f4 v[48:51], v[242:249], v[184:191], v[48:51]
	v_mfma_f32_16x16x128_f8f6f4 v[36:39], v[234:241], v[196:203], v[36:39]
	v_mfma_f32_16x16x128_f8f6f4 v[32:35], v[242:249], v[196:203], v[32:35]
	v_mfma_f32_16x16x128_f8f6f4 v[20:23], v[234:241], v[204:211], v[20:23]
	v_mfma_f32_16x16x128_f8f6f4 v[16:19], v[242:249], v[204:211], v[16:19]
	v_mfma_f32_16x16x128_f8f6f4 v[4:7], v[234:241], v[212:219], v[4:7]
	v_mfma_f32_16x16x128_f8f6f4 v[0:3], v[242:249], v[212:219], v[0:3]
	s_setprio 0
	s_barrier
	ds_read_b128 v[168:171], v154 offset:32768
	ds_read_b128 v[176:179], v154 offset:34816
	ds_read_b128 v[172:175], v155 offset:32768
	ds_read_b128 v[180:183], v155 offset:34816
	s_mov_b32 m0, s48
	ds_read_b128 v[184:187], v152 offset:32768
	ds_read_b128 v[196:199], v152 offset:34816
	ds_read_b128 v[188:191], v153 offset:32768
	ds_read_b128 v[200:203], v153 offset:34816
	ds_read_b128 v[204:207], v152 offset:36864
	ds_read_b128 v[212:215], v152 offset:38912
	ds_read_b128 v[208:211], v153 offset:36864
	ds_read_b128 v[216:219], v153 offset:38912
	v_cndmask_b32_e32 v132, v138, v165, vcc
	global_load_lds_dwordx4 v137, s[40:41]
	s_mov_b32 m0, s49
	s_nop 0
	global_load_lds_dwordx4 v132, s[40:41]
	s_waitcnt vmcnt(8)
	s_waitcnt lgkmcnt(8)
	s_barrier
	s_waitcnt lgkmcnt(0)
	s_setprio 1
	v_mfma_f32_16x16x128_f8f6f4 v[124:127], v[168:175], v[184:191], v[124:127]
	v_mfma_f32_16x16x128_f8f6f4 v[120:123], v[176:183], v[184:191], v[120:123]
	v_mfma_f32_16x16x128_f8f6f4 v[108:111], v[168:175], v[196:203], v[108:111]
	v_mfma_f32_16x16x128_f8f6f4 v[104:107], v[176:183], v[196:203], v[104:107]
	v_mfma_f32_16x16x128_f8f6f4 v[92:95], v[168:175], v[204:211], v[92:95]
	v_mfma_f32_16x16x128_f8f6f4 v[88:91], v[176:183], v[204:211], v[88:91]
	v_mfma_f32_16x16x128_f8f6f4 v[76:79], v[168:175], v[212:219], v[76:79]
	v_mfma_f32_16x16x128_f8f6f4 v[72:75], v[176:183], v[212:219], v[72:75]
	s_setprio 0
	s_barrier
	ds_read_b128 v[234:237], v154 offset:49152
	ds_read_b128 v[242:245], v154 offset:51200
	ds_read_b128 v[238:241], v155 offset:49152
	ds_read_b128 v[246:249], v155 offset:51200
	s_add_u32 s40, s38, 0x4000
	s_addc_u32 s41, s39, 0
	v_lshl_add_u64 v[192:193], s[40:41], 0, v[130:131]
	s_mov_b32 m0, s46
	s_nop 0
	global_load_lds_dwordx4 v[192:193], off
	v_lshl_add_u64 v[192:193], s[40:41], 0, v[128:129]
	s_mov_b32 m0, s47
	s_nop 0
	global_load_lds_dwordx4 v[192:193], off
	s_waitcnt vmcnt(8)
	s_barrier
	s_waitcnt lgkmcnt(0)
	s_setprio 1
	v_mfma_f32_16x16x128_f8f6f4 v[116:119], v[234:241], v[184:191], v[116:119]
	v_mfma_f32_16x16x128_f8f6f4 v[112:115], v[242:249], v[184:191], v[112:115]
	v_mfma_f32_16x16x128_f8f6f4 v[100:103], v[234:241], v[196:203], v[100:103]
	v_mfma_f32_16x16x128_f8f6f4 v[96:99], v[242:249], v[196:203], v[96:99]
	v_mfma_f32_16x16x128_f8f6f4 v[84:87], v[234:241], v[204:211], v[84:87]
	v_mfma_f32_16x16x128_f8f6f4 v[80:83], v[242:249], v[204:211], v[80:83]
	v_mfma_f32_16x16x128_f8f6f4 v[68:71], v[234:241], v[212:219], v[68:71]
	v_mfma_f32_16x16x128_f8f6f4 v[64:67], v[242:249], v[212:219], v[64:67]
	s_setprio 0
	s_barrier
	s_mov_b32 m0, s60
	v_lshl_add_u64 v[252:253], v[252:253], 0, s[16:17]
	ds_read_b128 v[184:187], v152 offset:49152
	ds_read_b128 v[196:199], v152 offset:51200
	ds_read_b128 v[188:191], v153 offset:49152
	ds_read_b128 v[200:203], v153 offset:51200
	ds_read_b128 v[204:207], v152 offset:53248
	ds_read_b128 v[212:215], v152 offset:55296
	ds_read_b128 v[208:211], v153 offset:53248
	ds_read_b128 v[216:219], v153 offset:55296
	global_load_lds_dwordx4 v[252:253], off
	v_lshl_add_u64 v[250:251], v[250:251], 0, s[16:17]
	s_mov_b32 m0, s61
	s_nop 0
	global_load_lds_dwordx4 v[250:251], off
	s_barrier
	s_waitcnt lgkmcnt(0)
	s_setprio 1
	v_mfma_f32_16x16x128_f8f6f4 v[60:63], v[168:175], v[184:191], v[60:63]
	v_mfma_f32_16x16x128_f8f6f4 v[56:59], v[176:183], v[184:191], v[56:59]
	v_mfma_f32_16x16x128_f8f6f4 v[44:47], v[168:175], v[196:203], v[44:47]
	v_mfma_f32_16x16x128_f8f6f4 v[40:43], v[176:183], v[196:203], v[40:43]
	v_mfma_f32_16x16x128_f8f6f4 v[28:31], v[168:175], v[204:211], v[28:31]
	v_mfma_f32_16x16x128_f8f6f4 v[24:27], v[176:183], v[204:211], v[24:27]
	v_mfma_f32_16x16x128_f8f6f4 v[12:15], v[168:175], v[212:219], v[12:15]
	v_mfma_f32_16x16x128_f8f6f4 v[8:11], v[176:183], v[212:219], v[8:11]
	s_setprio 0
	s_barrier
	s_mov_b32 m0, s58
	v_lshl_add_u64 v[144:145], v[144:145], 0, s[16:17]
	global_load_lds_dwordx4 v[144:145], off
	v_lshl_add_u64 v[144:145], v[146:147], 0, s[16:17]
	s_mov_b32 m0, s59
	s_nop 0
	global_load_lds_dwordx4 v[144:145], off
	s_waitcnt vmcnt(8)
	s_barrier
	s_setprio 1
	s_waitcnt lgkmcnt(0)
	v_mfma_f32_16x16x128_f8f6f4 v[52:55], v[234:241], v[184:191], v[52:55]
	v_mfma_f32_16x16x128_f8f6f4 v[48:51], v[242:249], v[184:191], v[48:51]
	v_mfma_f32_16x16x128_f8f6f4 v[36:39], v[234:241], v[196:203], v[36:39]
	v_mfma_f32_16x16x128_f8f6f4 v[32:35], v[242:249], v[196:203], v[32:35]
	v_mfma_f32_16x16x128_f8f6f4 v[20:23], v[234:241], v[204:211], v[20:23]
	v_mfma_f32_16x16x128_f8f6f4 v[16:19], v[242:249], v[204:211], v[16:19]
	v_mfma_f32_16x16x128_f8f6f4 v[4:7], v[234:241], v[212:219], v[4:7]
	v_mfma_f32_16x16x128_f8f6f4 v[0:3], v[242:249], v[212:219], v[0:3]
	s_setprio 0
	s_barrier
	s_add_u32 s38, s38, 0x4080
	s_addc_u32 s39, s39, 0
	s_mov_b32 m0, s62
	v_lshl_add_u64 v[144:145], s[38:39], 0, v[130:131]
	global_load_lds_dwordx4 v[144:145], off
	v_lshl_add_u64 v[144:145], s[38:39], 0, v[128:129]
	s_mov_b32 m0, s63
	s_add_i32 s57, s57, 2
	global_load_lds_dwordx4 v[144:145], off
	s_add_u32 s36, s36, 0x100
	s_addc_u32 s37, s37, 0
	s_cmp_gt_u32 s57, 13
	s_cbranch_scc0 .LBB0_756
	s_and_b64 vcc, exec, s[20:21]
	s_cbranch_vccz .LBB0_759
	s_barrier

.LBB0_1060:
	v_mov_b32_e32 v137, v133
	v_mov_b32_e32 v139, v133
	s_mov_b64 s[44:45], 0
	s_mov_b64 s[40:41], -1
	s_mov_b64 s[42:43], 0
	s_add_u32 s52, s12, s44
	s_addc_u32 s53, s13, s45
	s_add_u32 s29, s52, 0x100
	s_addc_u32 s48, s53, 0
	s_and_b64 s[46:47], s[42:43], exec
	s_cselect_b32 s46, s12, s29
	s_cselect_b32 s47, s13, s48
	s_add_u32 s29, s38, s44
	s_addc_u32 s44, s39, s45
	s_add_u32 s29, s29, 0x100
	s_addc_u32 s48, s44, 0
	ds_read_b128 v[162:165], v147
	ds_read_b128 v[170:173], v147 offset:2048
	ds_read_b128 v[166:169], v148
	ds_read_b128 v[174:177], v148 offset:2048
	s_and_b64 s[44:45], s[42:43], exec
	s_cselect_b32 s51, s35, s48
	s_cselect_b32 s50, s34, s29
	ds_read_b128 v[178:181], v145
	ds_read_b128 v[186:189], v145 offset:2048
	ds_read_b128 v[182:185], v146
	ds_read_b128 v[190:193], v146 offset:2048
	ds_read_b128 v[196:199], v145 offset:4096
	ds_read_b128 v[204:207], v145 offset:6144
	ds_read_b128 v[200:203], v146 offset:4096
	ds_read_b128 v[208:211], v146 offset:6144
	s_waitcnt vmcnt(6)
	s_waitcnt lgkmcnt(8)
	s_barrier
	s_waitcnt lgkmcnt(0)
	v_cndmask_b32_e64 v140, v134, v158, s[42:43]
	s_setprio 1
	s_waitcnt lgkmcnt(0)
	v_mfma_f32_16x16x128_f8f6f4 v[124:127], v[162:169], v[178:185], 0
	v_mfma_f32_16x16x128_f8f6f4 v[120:123], v[170:177], v[178:185], 0
	v_mfma_f32_16x16x128_f8f6f4 v[108:111], v[162:169], v[186:193], 0
	v_mfma_f32_16x16x128_f8f6f4 v[104:107], v[170:177], v[186:193], 0
	v_mfma_f32_16x16x128_f8f6f4 v[92:95], v[162:169], v[196:203], 0
	v_mfma_f32_16x16x128_f8f6f4 v[88:91], v[170:177], v[196:203], 0
	v_mfma_f32_16x16x128_f8f6f4 v[76:79], v[162:169], v[204:211], 0
	v_mfma_f32_16x16x128_f8f6f4 v[72:75], v[170:177], v[204:211], 0
	s_setprio 0
	s_barrier
	ds_read_b128 v[218:221], v147 offset:16384
	ds_read_b128 v[226:229], v147 offset:18432
	ds_read_b128 v[222:225], v148 offset:16384
	ds_read_b128 v[230:233], v148 offset:18432
	s_add_i32 m0, s0, 0xc000
	s_add_i32 s29, s0, 0xe000
	s_add_u32 s48, s50, 0x1000
	s_addc_u32 s49, s51, 0
	s_add_u32 s44, s50, 0x1080
	s_addc_u32 s45, s51, 0
	v_cndmask_b32_e64 v132, v135, v157, s[42:43]
	v_cndmask_b32_e64 v161, v136, v159, s[42:43]
	v_lshl_add_u64 v[252:253], s[52:53], 0, v[136:137]
	v_lshl_add_u64 v[252:253], v[252:253], 0, s[20:21]
	global_load_lds_dwordx4 v[252:253], off
	v_lshl_add_u64 v[252:253], s[52:53], 0, v[138:139]
	v_lshl_add_u64 v[252:253], v[252:253], 0, s[20:21]
	s_mov_b32 m0, s29
	s_nop 0
	global_load_lds_dwordx4 v[252:253], off
	s_barrier
	s_waitcnt lgkmcnt(0)
	s_setprio 1
	v_mfma_f32_16x16x128_f8f6f4 v[116:119], v[218:225], v[178:185], 0
	v_mfma_f32_16x16x128_f8f6f4 v[112:115], v[226:233], v[178:185], 0
	v_mfma_f32_16x16x128_f8f6f4 v[100:103], v[218:225], v[186:193], 0
	v_mfma_f32_16x16x128_f8f6f4 v[96:99], v[226:233], v[186:193], 0
	v_mfma_f32_16x16x128_f8f6f4 v[84:87], v[218:225], v[196:203], 0
	v_mfma_f32_16x16x128_f8f6f4 v[80:83], v[226:233], v[196:203], 0
	v_mfma_f32_16x16x128_f8f6f4 v[68:71], v[218:225], v[204:211], 0
	v_mfma_f32_16x16x128_f8f6f4 v[64:67], v[226:233], v[204:211], 0
	s_setprio 0
	s_barrier
	s_mov_b32 m0, s0
	ds_read_b128 v[178:181], v145 offset:16384
	ds_read_b128 v[186:189], v145 offset:18432
	ds_read_b128 v[182:185], v146 offset:16384
	ds_read_b128 v[190:193], v146 offset:18432
	ds_read_b128 v[196:199], v145 offset:20480
	ds_read_b128 v[204:207], v145 offset:22528
	ds_read_b128 v[200:203], v146 offset:20480
	ds_read_b128 v[208:211], v146 offset:22528
	global_load_lds_dwordx4 v132, s[46:47]
	s_mov_b32 m0, s56
	v_mov_b32_e32 v141, v133
	global_load_lds_dwordx4 v140, s[46:47]
	s_barrier
	s_waitcnt lgkmcnt(0)
	v_lshl_add_u64 v[212:213], s[46:47], 0, v[132:133]
	v_lshl_add_u64 v[214:215], s[46:47], 0, v[140:141]
	s_setprio 1
	s_waitcnt lgkmcnt(0)
	v_mfma_f32_16x16x128_f8f6f4 v[60:63], v[162:169], v[178:185], 0
	v_mfma_f32_16x16x128_f8f6f4 v[56:59], v[170:177], v[178:185], 0
	v_mfma_f32_16x16x128_f8f6f4 v[44:47], v[162:169], v[186:193], 0
	v_mfma_f32_16x16x128_f8f6f4 v[40:43], v[170:177], v[186:193], 0
	v_mfma_f32_16x16x128_f8f6f4 v[28:31], v[162:169], v[196:203], 0
	v_mfma_f32_16x16x128_f8f6f4 v[24:27], v[170:177], v[196:203], 0
	v_mfma_f32_16x16x128_f8f6f4 v[12:15], v[162:169], v[204:211], 0
	v_mfma_f32_16x16x128_f8f6f4 v[8:11], v[170:177], v[204:211], 0
	s_setprio 0
	s_barrier
	s_mov_b32 m0, s1
	v_lshl_add_u64 v[140:141], s[50:51], 0, v[128:129]
	global_load_lds_dwordx4 v[140:141], off
	v_lshl_add_u64 v[142:143], s[50:51], 0, v[130:131]
	s_mov_b32 m0, s37
	s_nop 0
	global_load_lds_dwordx4 v[142:143], off
	s_waitcnt vmcnt(8)
	s_barrier
	s_setprio 1
	s_waitcnt lgkmcnt(0)
	v_mfma_f32_16x16x128_f8f6f4 v[52:55], v[218:225], v[178:185], 0
	v_mfma_f32_16x16x128_f8f6f4 v[48:51], v[226:233], v[178:185], 0
	v_mfma_f32_16x16x128_f8f6f4 v[36:39], v[218:225], v[186:193], 0
	v_mfma_f32_16x16x128_f8f6f4 v[32:35], v[226:233], v[186:193], 0
	v_mfma_f32_16x16x128_f8f6f4 v[20:23], v[218:225], v[196:203], 0
	v_mfma_f32_16x16x128_f8f6f4 v[16:19], v[226:233], v[196:203], 0
	v_mfma_f32_16x16x128_f8f6f4 v[4:7], v[218:225], v[204:211], 0
	v_mfma_f32_16x16x128_f8f6f4 v[0:3], v[226:233], v[204:211], 0
	s_setprio 0
	s_barrier
	ds_read_b128 v[162:165], v147 offset:32768
	ds_read_b128 v[170:173], v147 offset:34816
	ds_read_b128 v[166:169], v148 offset:32768
	ds_read_b128 v[174:177], v148 offset:34816
	s_mov_b32 m0, s63
	ds_read_b128 v[178:181], v145 offset:32768
	ds_read_b128 v[186:189], v145 offset:34816
	ds_read_b128 v[182:185], v146 offset:32768
	ds_read_b128 v[190:193], v146 offset:34816
	ds_read_b128 v[196:199], v145 offset:36864
	ds_read_b128 v[204:207], v145 offset:38912
	ds_read_b128 v[200:203], v146 offset:36864
	ds_read_b128 v[208:211], v146 offset:38912
	v_cndmask_b32_e64 v132, v138, v160, s[42:43]
	global_load_lds_dwordx4 v161, s[46:47]
	s_mov_b32 m0, s64
	s_nop 0
	global_load_lds_dwordx4 v132, s[46:47]
	s_waitcnt vmcnt(8)
	s_waitcnt lgkmcnt(8)
	s_barrier
	s_waitcnt lgkmcnt(0)
	s_setprio 1
	v_mfma_f32_16x16x128_f8f6f4 v[124:127], v[162:169], v[178:185], v[124:127]
	v_mfma_f32_16x16x128_f8f6f4 v[120:123], v[170:177], v[178:185], v[120:123]
	v_mfma_f32_16x16x128_f8f6f4 v[108:111], v[162:169], v[186:193], v[108:111]
	v_mfma_f32_16x16x128_f8f6f4 v[104:107], v[170:177], v[186:193], v[104:107]
	v_mfma_f32_16x16x128_f8f6f4 v[92:95], v[162:169], v[196:203], v[92:95]
	v_mfma_f32_16x16x128_f8f6f4 v[88:91], v[170:177], v[196:203], v[88:91]
	v_mfma_f32_16x16x128_f8f6f4 v[76:79], v[162:169], v[204:211], v[76:79]
	v_mfma_f32_16x16x128_f8f6f4 v[72:75], v[170:177], v[204:211], v[72:75]
	s_setprio 0
	s_barrier
	ds_read_b128 v[218:221], v147 offset:49152
	ds_read_b128 v[226:229], v147 offset:51200
	ds_read_b128 v[222:225], v148 offset:49152
	ds_read_b128 v[230:233], v148 offset:51200
	v_lshl_add_u64 v[216:217], s[48:49], 0, v[128:129]
	s_mov_b32 m0, s57
	s_nop 0
	global_load_lds_dwordx4 v[216:217], off
	v_lshl_add_u64 v[216:217], s[48:49], 0, v[130:131]
	s_mov_b32 m0, s62
	s_nop 0
	global_load_lds_dwordx4 v[216:217], off
	s_waitcnt vmcnt(8)
	s_barrier
	s_waitcnt lgkmcnt(0)
	s_setprio 1
	v_mfma_f32_16x16x128_f8f6f4 v[116:119], v[218:225], v[178:185], v[116:119]
	v_mfma_f32_16x16x128_f8f6f4 v[112:115], v[226:233], v[178:185], v[112:115]
	v_mfma_f32_16x16x128_f8f6f4 v[100:103], v[218:225], v[186:193], v[100:103]
	v_mfma_f32_16x16x128_f8f6f4 v[96:99], v[226:233], v[186:193], v[96:99]
	v_mfma_f32_16x16x128_f8f6f4 v[84:87], v[218:225], v[196:203], v[84:87]
	v_mfma_f32_16x16x128_f8f6f4 v[80:83], v[226:233], v[196:203], v[80:83]
	v_mfma_f32_16x16x128_f8f6f4 v[68:71], v[218:225], v[204:211], v[68:71]
	v_mfma_f32_16x16x128_f8f6f4 v[64:67], v[226:233], v[204:211], v[64:67]
	s_setprio 0
	s_barrier
	s_mov_b32 m0, s67
	v_lshl_add_u64 v[212:213], v[212:213], 0, s[20:21]
	ds_read_b128 v[178:181], v145 offset:49152
	ds_read_b128 v[186:189], v145 offset:51200
	ds_read_b128 v[182:185], v146 offset:49152
	ds_read_b128 v[190:193], v146 offset:51200
	ds_read_b128 v[196:199], v145 offset:53248
	ds_read_b128 v[204:207], v145 offset:55296
	ds_read_b128 v[200:203], v146 offset:53248
	ds_read_b128 v[208:211], v146 offset:55296
	global_load_lds_dwordx4 v[212:213], off
	v_lshl_add_u64 v[212:213], v[214:215], 0, s[20:21]
	s_mov_b32 m0, s68
	s_nop 0
	global_load_lds_dwordx4 v[212:213], off
	s_barrier
	s_waitcnt lgkmcnt(0)
	s_setprio 1
	v_mfma_f32_16x16x128_f8f6f4 v[60:63], v[162:169], v[178:185], v[60:63]
	v_mfma_f32_16x16x128_f8f6f4 v[56:59], v[170:177], v[178:185], v[56:59]
	v_mfma_f32_16x16x128_f8f6f4 v[44:47], v[162:169], v[186:193], v[44:47]
	v_mfma_f32_16x16x128_f8f6f4 v[40:43], v[170:177], v[186:193], v[40:43]
	v_mfma_f32_16x16x128_f8f6f4 v[28:31], v[162:169], v[196:203], v[28:31]
	v_mfma_f32_16x16x128_f8f6f4 v[24:27], v[170:177], v[196:203], v[24:27]
	v_mfma_f32_16x16x128_f8f6f4 v[12:15], v[162:169], v[204:211], v[12:15]
	v_mfma_f32_16x16x128_f8f6f4 v[8:11], v[170:177], v[204:211], v[8:11]
	s_setprio 0
	s_barrier
	s_mov_b32 m0, s65
	v_lshl_add_u64 v[140:141], v[140:141], 0, s[20:21]
	global_load_lds_dwordx4 v[140:141], off
	v_lshl_add_u64 v[140:141], v[142:143], 0, s[20:21]
	s_mov_b32 m0, s66
	s_nop 0
	global_load_lds_dwordx4 v[140:141], off
	s_waitcnt vmcnt(8)
	s_barrier
	s_setprio 1
	s_waitcnt lgkmcnt(0)
	v_mfma_f32_16x16x128_f8f6f4 v[52:55], v[218:225], v[178:185], v[52:55]
	v_mfma_f32_16x16x128_f8f6f4 v[48:51], v[226:233], v[178:185], v[48:51]
	v_mfma_f32_16x16x128_f8f6f4 v[36:39], v[218:225], v[186:193], v[36:39]
	v_mfma_f32_16x16x128_f8f6f4 v[32:35], v[226:233], v[186:193], v[32:35]
	v_mfma_f32_16x16x128_f8f6f4 v[20:23], v[218:225], v[196:203], v[20:23]
	v_mfma_f32_16x16x128_f8f6f4 v[16:19], v[226:233], v[196:203], v[16:19]
	v_mfma_f32_16x16x128_f8f6f4 v[4:7], v[218:225], v[204:211], v[4:7]
	v_mfma_f32_16x16x128_f8f6f4 v[0:3], v[226:233], v[204:211], v[0:3]
	s_setprio 0
	s_barrier
	s_mov_b32 m0, s69
	v_lshl_add_u64 v[140:141], s[44:45], 0, v[128:129]
	global_load_lds_dwordx4 v[140:141], off
	v_lshl_add_u64 v[140:141], s[44:45], 0, v[130:131]
	s_mov_b32 m0, s70
	s_andn2_b64 vcc, exec, s[40:41]
	global_load_lds_dwordx4 v[140:141], off
	s_mov_b64 s[42:43], -1
	s_mov_b64 s[40:41], 0
	s_mov_b64 s[44:45], 0x100
	s_cbranch_vccz .LBB0_1061
	s_branch .Lpeel_after_1061
.LBB0_1061:
	s_add_u32 s52, s12, s44
	s_addc_u32 s53, s13, s45
	s_add_u32 s29, s52, 0x100
	s_addc_u32 s48, s53, 0
	s_and_b64 s[46:47], s[42:43], exec
	s_cselect_b32 s46, s12, s29
	s_cselect_b32 s47, s13, s48
	s_add_u32 s29, s38, s44
	s_addc_u32 s44, s39, s45
	s_add_u32 s29, s29, 0x100
	s_addc_u32 s48, s44, 0
	ds_read_b128 v[162:165], v147
	ds_read_b128 v[170:173], v147 offset:2048
	ds_read_b128 v[166:169], v148
	ds_read_b128 v[174:177], v148 offset:2048
	s_and_b64 s[44:45], s[42:43], exec
	s_cselect_b32 s51, s35, s48
	s_cselect_b32 s50, s34, s29
	ds_read_b128 v[178:181], v145
	ds_read_b128 v[186:189], v145 offset:2048
	ds_read_b128 v[182:185], v146
	ds_read_b128 v[190:193], v146 offset:2048
	ds_read_b128 v[196:199], v145 offset:4096
	ds_read_b128 v[204:207], v145 offset:6144
	ds_read_b128 v[200:203], v146 offset:4096
	ds_read_b128 v[208:211], v146 offset:6144
	s_waitcnt vmcnt(6)
	s_waitcnt lgkmcnt(8)
	s_barrier
	s_waitcnt lgkmcnt(0)
	v_cndmask_b32_e64 v140, v134, v158, s[42:43]
	s_setprio 1
	s_waitcnt lgkmcnt(0)
	v_mfma_f32_16x16x128_f8f6f4 v[124:127], v[162:169], v[178:185], v[124:127]
	v_mfma_f32_16x16x128_f8f6f4 v[120:123], v[170:177], v[178:185], v[120:123]
	v_mfma_f32_16x16x128_f8f6f4 v[108:111], v[162:169], v[186:193], v[108:111]
	v_mfma_f32_16x16x128_f8f6f4 v[104:107], v[170:177], v[186:193], v[104:107]
	v_mfma_f32_16x16x128_f8f6f4 v[92:95], v[162:169], v[196:203], v[92:95]
	v_mfma_f32_16x16x128_f8f6f4 v[88:91], v[170:177], v[196:203], v[88:91]
	v_mfma_f32_16x16x128_f8f6f4 v[76:79], v[162:169], v[204:211], v[76:79]
	v_mfma_f32_16x16x128_f8f6f4 v[72:75], v[170:177], v[204:211], v[72:75]
	s_setprio 0
	s_barrier
	ds_read_b128 v[218:221], v147 offset:16384
	ds_read_b128 v[226:229], v147 offset:18432
	ds_read_b128 v[222:225], v148 offset:16384
	ds_read_b128 v[230:233], v148 offset:18432
	s_add_i32 m0, s0, 0xc000
	s_add_i32 s29, s0, 0xe000
	s_add_u32 s48, s50, 0x1000
	s_addc_u32 s49, s51, 0
	s_add_u32 s44, s50, 0x1080
	s_addc_u32 s45, s51, 0
	v_cndmask_b32_e64 v132, v135, v157, s[42:43]
	v_cndmask_b32_e64 v161, v136, v159, s[42:43]
	v_lshl_add_u64 v[252:253], s[52:53], 0, v[136:137]
	v_lshl_add_u64 v[252:253], v[252:253], 0, s[20:21]
	global_load_lds_dwordx4 v[252:253], off
	v_lshl_add_u64 v[252:253], s[52:53], 0, v[138:139]
	v_lshl_add_u64 v[252:253], v[252:253], 0, s[20:21]
	s_mov_b32 m0, s29
	s_nop 0
	global_load_lds_dwordx4 v[252:253], off
	s_barrier
	s_waitcnt lgkmcnt(0)
	s_setprio 1
	v_mfma_f32_16x16x128_f8f6f4 v[116:119], v[218:225], v[178:185], v[116:119]
	v_mfma_f32_16x16x128_f8f6f4 v[112:115], v[226:233], v[178:185], v[112:115]
	v_mfma_f32_16x16x128_f8f6f4 v[100:103], v[218:225], v[186:193], v[100:103]
	v_mfma_f32_16x16x128_f8f6f4 v[96:99], v[226:233], v[186:193], v[96:99]
	v_mfma_f32_16x16x128_f8f6f4 v[84:87], v[218:225], v[196:203], v[84:87]
	v_mfma_f32_16x16x128_f8f6f4 v[80:83], v[226:233], v[196:203], v[80:83]
	v_mfma_f32_16x16x128_f8f6f4 v[68:71], v[218:225], v[204:211], v[68:71]
	v_mfma_f32_16x16x128_f8f6f4 v[64:67], v[226:233], v[204:211], v[64:67]
	s_setprio 0
	s_barrier
	s_mov_b32 m0, s0
	ds_read_b128 v[178:181], v145 offset:16384
	ds_read_b128 v[186:189], v145 offset:18432
	ds_read_b128 v[182:185], v146 offset:16384
	ds_read_b128 v[190:193], v146 offset:18432
	ds_read_b128 v[196:199], v145 offset:20480
	ds_read_b128 v[204:207], v145 offset:22528
	ds_read_b128 v[200:203], v146 offset:20480
	ds_read_b128 v[208:211], v146 offset:22528
	global_load_lds_dwordx4 v132, s[46:47]
	s_mov_b32 m0, s56
	v_mov_b32_e32 v141, v133
	global_load_lds_dwordx4 v140, s[46:47]
	s_barrier
	s_waitcnt lgkmcnt(0)
	v_lshl_add_u64 v[212:213], s[46:47], 0, v[132:133]
	v_lshl_add_u64 v[214:215], s[46:47], 0, v[140:141]
	s_setprio 1
	s_waitcnt lgkmcnt(0)
	v_mfma_f32_16x16x128_f8f6f4 v[60:63], v[162:169], v[178:185], v[60:63]
	v_mfma_f32_16x16x128_f8f6f4 v[56:59], v[170:177], v[178:185], v[56:59]
	v_mfma_f32_16x16x128_f8f6f4 v[44:47], v[162:169], v[186:193], v[44:47]
	v_mfma_f32_16x16x128_f8f6f4 v[40:43], v[170:177], v[186:193], v[40:43]
	v_mfma_f32_16x16x128_f8f6f4 v[28:31], v[162:169], v[196:203], v[28:31]
	v_mfma_f32_16x16x128_f8f6f4 v[24:27], v[170:177], v[196:203], v[24:27]
	v_mfma_f32_16x16x128_f8f6f4 v[12:15], v[162:169], v[204:211], v[12:15]
	v_mfma_f32_16x16x128_f8f6f4 v[8:11], v[170:177], v[204:211], v[8:11]
	s_setprio 0
	s_barrier
	s_mov_b32 m0, s1
	v_lshl_add_u64 v[140:141], s[50:51], 0, v[128:129]
	global_load_lds_dwordx4 v[140:141], off
	v_lshl_add_u64 v[142:143], s[50:51], 0, v[130:131]
	s_mov_b32 m0, s37
	s_nop 0
	global_load_lds_dwordx4 v[142:143], off
	s_waitcnt vmcnt(8)
	s_barrier
	s_setprio 1
	s_waitcnt lgkmcnt(0)
	v_mfma_f32_16x16x128_f8f6f4 v[52:55], v[218:225], v[178:185], v[52:55]
	v_mfma_f32_16x16x128_f8f6f4 v[48:51], v[226:233], v[178:185], v[48:51]
	v_mfma_f32_16x16x128_f8f6f4 v[36:39], v[218:225], v[186:193], v[36:39]
	v_mfma_f32_16x16x128_f8f6f4 v[32:35], v[226:233], v[186:193], v[32:35]
	v_mfma_f32_16x16x128_f8f6f4 v[20:23], v[218:225], v[196:203], v[20:23]
	v_mfma_f32_16x16x128_f8f6f4 v[16:19], v[226:233], v[196:203], v[16:19]
	v_mfma_f32_16x16x128_f8f6f4 v[4:7], v[218:225], v[204:211], v[4:7]
	v_mfma_f32_16x16x128_f8f6f4 v[0:3], v[226:233], v[204:211], v[0:3]
	s_setprio 0
	s_barrier
	ds_read_b128 v[162:165], v147 offset:32768
	ds_read_b128 v[170:173], v147 offset:34816
	ds_read_b128 v[166:169], v148 offset:32768
	ds_read_b128 v[174:177], v148 offset:34816
	s_mov_b32 m0, s63
	ds_read_b128 v[178:181], v145 offset:32768
	ds_read_b128 v[186:189], v145 offset:34816
	ds_read_b128 v[182:185], v146 offset:32768
	ds_read_b128 v[190:193], v146 offset:34816
	ds_read_b128 v[196:199], v145 offset:36864
	ds_read_b128 v[204:207], v145 offset:38912
	ds_read_b128 v[200:203], v146 offset:36864
	ds_read_b128 v[208:211], v146 offset:38912
	v_cndmask_b32_e64 v132, v138, v160, s[42:43]
	global_load_lds_dwordx4 v161, s[46:47]
	s_mov_b32 m0, s64
	s_nop 0
	global_load_lds_dwordx4 v132, s[46:47]
	s_waitcnt vmcnt(8)
	s_waitcnt lgkmcnt(8)
	s_barrier
	s_waitcnt lgkmcnt(0)
	s_setprio 1
	v_mfma_f32_16x16x128_f8f6f4 v[124:127], v[162:169], v[178:185], v[124:127]
	v_mfma_f32_16x16x128_f8f6f4 v[120:123], v[170:177], v[178:185], v[120:123]
	v_mfma_f32_16x16x128_f8f6f4 v[108:111], v[162:169], v[186:193], v[108:111]
	v_mfma_f32_16x16x128_f8f6f4 v[104:107], v[170:177], v[186:193], v[104:107]
	v_mfma_f32_16x16x128_f8f6f4 v[92:95], v[162:169], v[196:203], v[92:95]
	v_mfma_f32_16x16x128_f8f6f4 v[88:91], v[170:177], v[196:203], v[88:91]
	v_mfma_f32_16x16x128_f8f6f4 v[76:79], v[162:169], v[204:211], v[76:79]
	v_mfma_f32_16x16x128_f8f6f4 v[72:75], v[170:177], v[204:211], v[72:75]
	s_setprio 0
	s_barrier
	ds_read_b128 v[218:221], v147 offset:49152
	ds_read_b128 v[226:229], v147 offset:51200
	ds_read_b128 v[222:225], v148 offset:49152
	ds_read_b128 v[230:233], v148 offset:51200
	v_lshl_add_u64 v[216:217], s[48:49], 0, v[128:129]
	s_mov_b32 m0, s57
	s_nop 0
	global_load_lds_dwordx4 v[216:217], off
	v_lshl_add_u64 v[216:217], s[48:49], 0, v[130:131]
	s_mov_b32 m0, s62
	s_nop 0
	global_load_lds_dwordx4 v[216:217], off
	s_waitcnt vmcnt(8)
	s_barrier
	s_waitcnt lgkmcnt(0)
	s_setprio 1
	v_mfma_f32_16x16x128_f8f6f4 v[116:119], v[218:225], v[178:185], v[116:119]
	v_mfma_f32_16x16x128_f8f6f4 v[112:115], v[226:233], v[178:185], v[112:115]
	v_mfma_f32_16x16x128_f8f6f4 v[100:103], v[218:225], v[186:193], v[100:103]
	v_mfma_f32_16x16x128_f8f6f4 v[96:99], v[226:233], v[186:193], v[96:99]
	v_mfma_f32_16x16x128_f8f6f4 v[84:87], v[218:225], v[196:203], v[84:87]
	v_mfma_f32_16x16x128_f8f6f4 v[80:83], v[226:233], v[196:203], v[80:83]
	v_mfma_f32_16x16x128_f8f6f4 v[68:71], v[218:225], v[204:211], v[68:71]
	v_mfma_f32_16x16x128_f8f6f4 v[64:67], v[226:233], v[204:211], v[64:67]
	s_setprio 0
	s_barrier
	s_mov_b32 m0, s67
	v_lshl_add_u64 v[212:213], v[212:213], 0, s[20:21]
	ds_read_b128 v[178:181], v145 offset:49152
	ds_read_b128 v[186:189], v145 offset:51200
	ds_read_b128 v[182:185], v146 offset:49152
	ds_read_b128 v[190:193], v146 offset:51200
	ds_read_b128 v[196:199], v145 offset:53248
	ds_read_b128 v[204:207], v145 offset:55296
	ds_read_b128 v[200:203], v146 offset:53248
	ds_read_b128 v[208:211], v146 offset:55296
	global_load_lds_dwordx4 v[212:213], off
	v_lshl_add_u64 v[212:213], v[214:215], 0, s[20:21]
	s_mov_b32 m0, s68
	s_nop 0
	global_load_lds_dwordx4 v[212:213], off
	s_barrier
	s_waitcnt lgkmcnt(0)
	s_setprio 1
	v_mfma_f32_16x16x128_f8f6f4 v[60:63], v[162:169], v[178:185], v[60:63]
	v_mfma_f32_16x16x128_f8f6f4 v[56:59], v[170:177], v[178:185], v[56:59]
	v_mfma_f32_16x16x128_f8f6f4 v[44:47], v[162:169], v[186:193], v[44:47]
	v_mfma_f32_16x16x128_f8f6f4 v[40:43], v[170:177], v[186:193], v[40:43]
	v_mfma_f32_16x16x128_f8f6f4 v[28:31], v[162:169], v[196:203], v[28:31]
	v_mfma_f32_16x16x128_f8f6f4 v[24:27], v[170:177], v[196:203], v[24:27]
	v_mfma_f32_16x16x128_f8f6f4 v[12:15], v[162:169], v[204:211], v[12:15]
	v_mfma_f32_16x16x128_f8f6f4 v[8:11], v[170:177], v[204:211], v[8:11]
	s_setprio 0
	s_barrier
	s_mov_b32 m0, s65
	v_lshl_add_u64 v[140:141], v[140:141], 0, s[20:21]
	global_load_lds_dwordx4 v[140:141], off
	v_lshl_add_u64 v[140:141], v[142:143], 0, s[20:21]
	s_mov_b32 m0, s66
	s_nop 0
	global_load_lds_dwordx4 v[140:141], off
	s_waitcnt vmcnt(8)
	s_barrier
	s_setprio 1
	s_waitcnt lgkmcnt(0)
	v_mfma_f32_16x16x128_f8f6f4 v[52:55], v[218:225], v[178:185], v[52:55]
	v_mfma_f32_16x16x128_f8f6f4 v[48:51], v[226:233], v[178:185], v[48:51]
	v_mfma_f32_16x16x128_f8f6f4 v[36:39], v[218:225], v[186:193], v[36:39]
	v_mfma_f32_16x16x128_f8f6f4 v[32:35], v[226:233], v[186:193], v[32:35]
	v_mfma_f32_16x16x128_f8f6f4 v[20:23], v[218:225], v[196:203], v[20:23]
	v_mfma_f32_16x16x128_f8f6f4 v[16:19], v[226:233], v[196:203], v[16:19]
	v_mfma_f32_16x16x128_f8f6f4 v[4:7], v[218:225], v[204:211], v[4:7]
	v_mfma_f32_16x16x128_f8f6f4 v[0:3], v[226:233], v[204:211], v[0:3]
	s_setprio 0
	s_barrier
	s_mov_b32 m0, s69
	v_lshl_add_u64 v[140:141], s[44:45], 0, v[128:129]
	global_load_lds_dwordx4 v[140:141], off
	v_lshl_add_u64 v[140:141], s[44:45], 0, v[130:131]
	s_mov_b32 m0, s70
	s_andn2_b64 vcc, exec, s[40:41]
	global_load_lds_dwordx4 v[140:141], off
	s_mov_b64 s[42:43], -1
	s_mov_b64 s[40:41], 0
	s_mov_b64 s[44:45], 0x100
	s_cbranch_vccz .LBB0_1061

.LBB0_1080:
	v_mov_b32_e32 v137, v133
	v_mov_b32_e32 v139, v133
	s_mov_b64 s[34:35], 0
	s_mov_b64 s[28:29], -1
	s_mov_b64 s[30:31], 0
	s_add_u32 s42, s10, s34
	s_addc_u32 s43, s11, s35
	s_add_u32 s38, s42, 0x100
	s_addc_u32 s39, s43, 0
	s_and_b64 s[36:37], s[30:31], exec
	s_cselect_b32 s36, s10, s38
	s_cselect_b32 s37, s11, s39
	s_add_u32 s34, s26, s34
	s_addc_u32 s35, s27, s35
	s_add_u32 s38, s34, 0x100
	s_addc_u32 s39, s35, 0
	ds_read_b128 v[160:163], v147
	ds_read_b128 v[168:171], v147 offset:2048
	ds_read_b128 v[164:167], v148
	ds_read_b128 v[172:175], v148 offset:2048
	s_and_b64 s[34:35], s[30:31], exec
	s_cselect_b32 s41, s25, s39
	s_cselect_b32 s40, s24, s38
	ds_read_b128 v[176:179], v145
	ds_read_b128 v[184:187], v145 offset:2048
	ds_read_b128 v[180:183], v146
	ds_read_b128 v[188:191], v146 offset:2048
	ds_read_b128 v[196:199], v145 offset:4096
	ds_read_b128 v[204:207], v145 offset:6144
	ds_read_b128 v[200:203], v146 offset:4096
	ds_read_b128 v[208:211], v146 offset:6144
	s_waitcnt vmcnt(6)
	s_waitcnt lgkmcnt(8)
	s_barrier
	s_waitcnt lgkmcnt(0)
	v_cndmask_b32_e64 v140, v134, v156, s[30:31]
	s_setprio 1
	s_waitcnt lgkmcnt(0)
	v_mfma_f32_16x16x128_f8f6f4 v[124:127], v[160:167], v[176:183], 0
	v_mfma_f32_16x16x128_f8f6f4 v[120:123], v[168:175], v[176:183], 0
	v_mfma_f32_16x16x128_f8f6f4 v[108:111], v[160:167], v[184:191], 0
	v_mfma_f32_16x16x128_f8f6f4 v[104:107], v[168:175], v[184:191], 0
	v_mfma_f32_16x16x128_f8f6f4 v[92:95], v[160:167], v[196:203], 0
	v_mfma_f32_16x16x128_f8f6f4 v[88:91], v[168:175], v[196:203], 0
	v_mfma_f32_16x16x128_f8f6f4 v[76:79], v[160:167], v[204:211], 0
	v_mfma_f32_16x16x128_f8f6f4 v[72:75], v[168:175], v[204:211], 0
	s_setprio 0
	s_barrier
	ds_read_b128 v[218:221], v147 offset:16384
	ds_read_b128 v[226:229], v147 offset:18432
	ds_read_b128 v[222:225], v148 offset:16384
	ds_read_b128 v[230:233], v148 offset:18432
	s_add_i32 m0, s1, 0xc000
	s_add_i32 s64, s1, 0xe000
	s_add_u32 s38, s40, 0x1000
	s_addc_u32 s39, s41, 0
	s_add_u32 s34, s40, 0x1080
	s_addc_u32 s35, s41, 0
	v_cndmask_b32_e64 v132, v135, v155, s[30:31]
	v_cndmask_b32_e64 v159, v136, v157, s[30:31]
	v_lshl_add_u64 v[252:253], s[42:43], 0, v[136:137]
	v_lshl_add_u64 v[252:253], v[252:253], 0, s[16:17]
	global_load_lds_dwordx4 v[252:253], off
	v_lshl_add_u64 v[252:253], s[42:43], 0, v[138:139]
	v_lshl_add_u64 v[252:253], v[252:253], 0, s[16:17]
	s_mov_b32 m0, s64
	s_nop 0
	global_load_lds_dwordx4 v[252:253], off
	s_barrier
	s_waitcnt lgkmcnt(0)
	s_setprio 1
	v_mfma_f32_16x16x128_f8f6f4 v[116:119], v[218:225], v[176:183], 0
	v_mfma_f32_16x16x128_f8f6f4 v[112:115], v[226:233], v[176:183], 0
	v_mfma_f32_16x16x128_f8f6f4 v[100:103], v[218:225], v[184:191], 0
	v_mfma_f32_16x16x128_f8f6f4 v[96:99], v[226:233], v[184:191], 0
	v_mfma_f32_16x16x128_f8f6f4 v[84:87], v[218:225], v[196:203], 0
	v_mfma_f32_16x16x128_f8f6f4 v[80:83], v[226:233], v[196:203], 0
	v_mfma_f32_16x16x128_f8f6f4 v[68:71], v[218:225], v[204:211], 0
	v_mfma_f32_16x16x128_f8f6f4 v[64:67], v[226:233], v[204:211], 0
	s_setprio 0
	s_barrier
	s_mov_b32 m0, s1
	ds_read_b128 v[176:179], v145 offset:16384
	ds_read_b128 v[184:187], v145 offset:18432
	ds_read_b128 v[180:183], v146 offset:16384
	ds_read_b128 v[188:191], v146 offset:18432
	ds_read_b128 v[196:199], v145 offset:20480
	ds_read_b128 v[204:207], v145 offset:22528
	ds_read_b128 v[200:203], v146 offset:20480
	ds_read_b128 v[208:211], v146 offset:22528
	global_load_lds_dwordx4 v132, s[36:37]
	s_mov_b32 m0, s48
	v_mov_b32_e32 v141, v133
	global_load_lds_dwordx4 v140, s[36:37]
	s_barrier
	s_waitcnt lgkmcnt(0)
	v_lshl_add_u64 v[192:193], s[36:37], 0, v[132:133]
	v_lshl_add_u64 v[212:213], s[36:37], 0, v[140:141]
	s_setprio 1
	s_waitcnt lgkmcnt(0)
	v_mfma_f32_16x16x128_f8f6f4 v[60:63], v[160:167], v[176:183], 0
	v_mfma_f32_16x16x128_f8f6f4 v[56:59], v[168:175], v[176:183], 0
	v_mfma_f32_16x16x128_f8f6f4 v[44:47], v[160:167], v[184:191], 0
	v_mfma_f32_16x16x128_f8f6f4 v[40:43], v[168:175], v[184:191], 0
	v_mfma_f32_16x16x128_f8f6f4 v[28:31], v[160:167], v[196:203], 0
	v_mfma_f32_16x16x128_f8f6f4 v[24:27], v[168:175], v[196:203], 0
	v_mfma_f32_16x16x128_f8f6f4 v[12:15], v[160:167], v[204:211], 0
	v_mfma_f32_16x16x128_f8f6f4 v[8:11], v[168:175], v[204:211], 0
	s_setprio 0
	s_barrier
	s_mov_b32 m0, s46
	v_lshl_add_u64 v[140:141], s[40:41], 0, v[130:131]
	global_load_lds_dwordx4 v[140:141], off
	v_lshl_add_u64 v[142:143], s[40:41], 0, v[128:129]
	s_mov_b32 m0, s47
	s_nop 0
	global_load_lds_dwordx4 v[142:143], off
	s_waitcnt vmcnt(8)
	s_barrier
	s_setprio 1
	s_waitcnt lgkmcnt(0)
	v_mfma_f32_16x16x128_f8f6f4 v[52:55], v[218:225], v[176:183], 0
	v_mfma_f32_16x16x128_f8f6f4 v[48:51], v[226:233], v[176:183], 0
	v_mfma_f32_16x16x128_f8f6f4 v[36:39], v[218:225], v[184:191], 0
	v_mfma_f32_16x16x128_f8f6f4 v[32:35], v[226:233], v[184:191], 0
	v_mfma_f32_16x16x128_f8f6f4 v[20:23], v[218:225], v[196:203], 0
	v_mfma_f32_16x16x128_f8f6f4 v[16:19], v[226:233], v[196:203], 0
	v_mfma_f32_16x16x128_f8f6f4 v[4:7], v[218:225], v[204:211], 0
	v_mfma_f32_16x16x128_f8f6f4 v[0:3], v[226:233], v[204:211], 0
	s_setprio 0
	s_barrier
	ds_read_b128 v[160:163], v147 offset:32768
	ds_read_b128 v[168:171], v147 offset:34816
	ds_read_b128 v[164:167], v148 offset:32768
	ds_read_b128 v[172:175], v148 offset:34816
	s_mov_b32 m0, s51
	ds_read_b128 v[176:179], v145 offset:32768
	ds_read_b128 v[184:187], v145 offset:34816
	ds_read_b128 v[180:183], v146 offset:32768
	ds_read_b128 v[188:191], v146 offset:34816
	ds_read_b128 v[196:199], v145 offset:36864
	ds_read_b128 v[204:207], v145 offset:38912
	ds_read_b128 v[200:203], v146 offset:36864
	ds_read_b128 v[208:211], v146 offset:38912
	v_cndmask_b32_e64 v132, v138, v158, s[30:31]
	global_load_lds_dwordx4 v159, s[36:37]
	s_mov_b32 m0, s52
	s_nop 0
	global_load_lds_dwordx4 v132, s[36:37]
	s_waitcnt vmcnt(8)
	s_waitcnt lgkmcnt(8)
	s_barrier
	s_waitcnt lgkmcnt(0)
	s_setprio 1
	v_mfma_f32_16x16x128_f8f6f4 v[124:127], v[160:167], v[176:183], v[124:127]
	v_mfma_f32_16x16x128_f8f6f4 v[120:123], v[168:175], v[176:183], v[120:123]
	v_mfma_f32_16x16x128_f8f6f4 v[108:111], v[160:167], v[184:191], v[108:111]
	v_mfma_f32_16x16x128_f8f6f4 v[104:107], v[168:175], v[184:191], v[104:107]
	v_mfma_f32_16x16x128_f8f6f4 v[92:95], v[160:167], v[196:203], v[92:95]
	v_mfma_f32_16x16x128_f8f6f4 v[88:91], v[168:175], v[196:203], v[88:91]
	v_mfma_f32_16x16x128_f8f6f4 v[76:79], v[160:167], v[204:211], v[76:79]
	v_mfma_f32_16x16x128_f8f6f4 v[72:75], v[168:175], v[204:211], v[72:75]
	s_setprio 0
	s_barrier
	ds_read_b128 v[218:221], v147 offset:49152
	ds_read_b128 v[226:229], v147 offset:51200
	ds_read_b128 v[222:225], v148 offset:49152
	ds_read_b128 v[230:233], v148 offset:51200
	v_lshl_add_u64 v[214:215], s[38:39], 0, v[130:131]
	s_mov_b32 m0, s49
	s_nop 0
	global_load_lds_dwordx4 v[214:215], off
	v_lshl_add_u64 v[214:215], s[38:39], 0, v[128:129]
	s_mov_b32 m0, s50
	s_nop 0
	global_load_lds_dwordx4 v[214:215], off
	s_waitcnt vmcnt(8)
	s_barrier
	s_waitcnt lgkmcnt(0)
	s_setprio 1
	v_mfma_f32_16x16x128_f8f6f4 v[116:119], v[218:225], v[176:183], v[116:119]
	v_mfma_f32_16x16x128_f8f6f4 v[112:115], v[226:233], v[176:183], v[112:115]
	v_mfma_f32_16x16x128_f8f6f4 v[100:103], v[218:225], v[184:191], v[100:103]
	v_mfma_f32_16x16x128_f8f6f4 v[96:99], v[226:233], v[184:191], v[96:99]
	v_mfma_f32_16x16x128_f8f6f4 v[84:87], v[218:225], v[196:203], v[84:87]
	v_mfma_f32_16x16x128_f8f6f4 v[80:83], v[226:233], v[196:203], v[80:83]
	v_mfma_f32_16x16x128_f8f6f4 v[68:71], v[218:225], v[204:211], v[68:71]
	v_mfma_f32_16x16x128_f8f6f4 v[64:67], v[226:233], v[204:211], v[64:67]
	s_setprio 0
	s_barrier
	s_mov_b32 m0, s56
	v_lshl_add_u64 v[192:193], v[192:193], 0, s[16:17]
	ds_read_b128 v[176:179], v145 offset:49152
	ds_read_b128 v[184:187], v145 offset:51200
	ds_read_b128 v[180:183], v146 offset:49152
	ds_read_b128 v[188:191], v146 offset:51200
	ds_read_b128 v[196:199], v145 offset:53248
	ds_read_b128 v[204:207], v145 offset:55296
	ds_read_b128 v[200:203], v146 offset:53248
	ds_read_b128 v[208:211], v146 offset:55296
	global_load_lds_dwordx4 v[192:193], off
	v_lshl_add_u64 v[192:193], v[212:213], 0, s[16:17]
	s_mov_b32 m0, s57
	s_nop 0
	global_load_lds_dwordx4 v[192:193], off
	s_barrier
	s_waitcnt lgkmcnt(0)
	s_setprio 1
	v_mfma_f32_16x16x128_f8f6f4 v[60:63], v[160:167], v[176:183], v[60:63]
	v_mfma_f32_16x16x128_f8f6f4 v[56:59], v[168:175], v[176:183], v[56:59]
	v_mfma_f32_16x16x128_f8f6f4 v[44:47], v[160:167], v[184:191], v[44:47]
	v_mfma_f32_16x16x128_f8f6f4 v[40:43], v[168:175], v[184:191], v[40:43]
	v_mfma_f32_16x16x128_f8f6f4 v[28:31], v[160:167], v[196:203], v[28:31]
	v_mfma_f32_16x16x128_f8f6f4 v[24:27], v[168:175], v[196:203], v[24:27]
	v_mfma_f32_16x16x128_f8f6f4 v[12:15], v[160:167], v[204:211], v[12:15]
	v_mfma_f32_16x16x128_f8f6f4 v[8:11], v[168:175], v[204:211], v[8:11]
	s_setprio 0
	s_barrier
	s_mov_b32 m0, s54
	v_lshl_add_u64 v[140:141], v[140:141], 0, s[16:17]
	global_load_lds_dwordx4 v[140:141], off
	v_lshl_add_u64 v[140:141], v[142:143], 0, s[16:17]
	s_mov_b32 m0, s55
	s_nop 0
	global_load_lds_dwordx4 v[140:141], off
	s_waitcnt vmcnt(8)
	s_barrier
	s_setprio 1
	s_waitcnt lgkmcnt(0)
	v_mfma_f32_16x16x128_f8f6f4 v[52:55], v[218:225], v[176:183], v[52:55]
	v_mfma_f32_16x16x128_f8f6f4 v[48:51], v[226:233], v[176:183], v[48:51]
	v_mfma_f32_16x16x128_f8f6f4 v[36:39], v[218:225], v[184:191], v[36:39]
	v_mfma_f32_16x16x128_f8f6f4 v[32:35], v[226:233], v[184:191], v[32:35]
	v_mfma_f32_16x16x128_f8f6f4 v[20:23], v[218:225], v[196:203], v[20:23]
	v_mfma_f32_16x16x128_f8f6f4 v[16:19], v[226:233], v[196:203], v[16:19]
	v_mfma_f32_16x16x128_f8f6f4 v[4:7], v[218:225], v[204:211], v[4:7]
	v_mfma_f32_16x16x128_f8f6f4 v[0:3], v[226:233], v[204:211], v[0:3]
	s_setprio 0
	s_barrier
	s_mov_b32 m0, s58
	v_lshl_add_u64 v[140:141], s[34:35], 0, v[130:131]
	global_load_lds_dwordx4 v[140:141], off
	v_lshl_add_u64 v[140:141], s[34:35], 0, v[128:129]
	s_mov_b32 m0, s59
	s_andn2_b64 vcc, exec, s[28:29]
	global_load_lds_dwordx4 v[140:141], off
	s_mov_b64 s[30:31], -1
	s_mov_b64 s[28:29], 0
	s_mov_b64 s[34:35], 0x100
	s_cbranch_vccz .LBB0_1081
	s_branch .Lpeel_after_1081
.LBB0_1081:
	s_add_u32 s42, s10, s34
	s_addc_u32 s43, s11, s35
	s_add_u32 s38, s42, 0x100
	s_addc_u32 s39, s43, 0
	s_and_b64 s[36:37], s[30:31], exec
	s_cselect_b32 s36, s10, s38
	s_cselect_b32 s37, s11, s39
	s_add_u32 s34, s26, s34
	s_addc_u32 s35, s27, s35
	s_add_u32 s38, s34, 0x100
	s_addc_u32 s39, s35, 0
	ds_read_b128 v[160:163], v147
	ds_read_b128 v[168:171], v147 offset:2048
	ds_read_b128 v[164:167], v148
	ds_read_b128 v[172:175], v148 offset:2048
	s_and_b64 s[34:35], s[30:31], exec
	s_cselect_b32 s41, s25, s39
	s_cselect_b32 s40, s24, s38
	ds_read_b128 v[176:179], v145
	ds_read_b128 v[184:187], v145 offset:2048
	ds_read_b128 v[180:183], v146
	ds_read_b128 v[188:191], v146 offset:2048
	ds_read_b128 v[196:199], v145 offset:4096
	ds_read_b128 v[204:207], v145 offset:6144
	ds_read_b128 v[200:203], v146 offset:4096
	ds_read_b128 v[208:211], v146 offset:6144
	s_waitcnt vmcnt(6)
	s_waitcnt lgkmcnt(8)
	s_barrier
	s_waitcnt lgkmcnt(0)
	v_cndmask_b32_e64 v140, v134, v156, s[30:31]
	s_setprio 1
	s_waitcnt lgkmcnt(0)
	v_mfma_f32_16x16x128_f8f6f4 v[124:127], v[160:167], v[176:183], v[124:127]
	v_mfma_f32_16x16x128_f8f6f4 v[120:123], v[168:175], v[176:183], v[120:123]
	v_mfma_f32_16x16x128_f8f6f4 v[108:111], v[160:167], v[184:191], v[108:111]
	v_mfma_f32_16x16x128_f8f6f4 v[104:107], v[168:175], v[184:191], v[104:107]
	v_mfma_f32_16x16x128_f8f6f4 v[92:95], v[160:167], v[196:203], v[92:95]
	v_mfma_f32_16x16x128_f8f6f4 v[88:91], v[168:175], v[196:203], v[88:91]
	v_mfma_f32_16x16x128_f8f6f4 v[76:79], v[160:167], v[204:211], v[76:79]
	v_mfma_f32_16x16x128_f8f6f4 v[72:75], v[168:175], v[204:211], v[72:75]
	s_setprio 0
	s_barrier
	ds_read_b128 v[218:221], v147 offset:16384
	ds_read_b128 v[226:229], v147 offset:18432
	ds_read_b128 v[222:225], v148 offset:16384
	ds_read_b128 v[230:233], v148 offset:18432
	s_add_i32 m0, s1, 0xc000
	s_add_i32 s64, s1, 0xe000
	s_add_u32 s38, s40, 0x1000
	s_addc_u32 s39, s41, 0
	s_add_u32 s34, s40, 0x1080
	s_addc_u32 s35, s41, 0
	v_cndmask_b32_e64 v132, v135, v155, s[30:31]
	v_cndmask_b32_e64 v159, v136, v157, s[30:31]
	v_lshl_add_u64 v[252:253], s[42:43], 0, v[136:137]
	v_lshl_add_u64 v[252:253], v[252:253], 0, s[16:17]
	global_load_lds_dwordx4 v[252:253], off
	v_lshl_add_u64 v[252:253], s[42:43], 0, v[138:139]
	v_lshl_add_u64 v[252:253], v[252:253], 0, s[16:17]
	s_mov_b32 m0, s64
	s_nop 0
	global_load_lds_dwordx4 v[252:253], off
	s_barrier
	s_waitcnt lgkmcnt(0)
	s_setprio 1
	v_mfma_f32_16x16x128_f8f6f4 v[116:119], v[218:225], v[176:183], v[116:119]
	v_mfma_f32_16x16x128_f8f6f4 v[112:115], v[226:233], v[176:183], v[112:115]
	v_mfma_f32_16x16x128_f8f6f4 v[100:103], v[218:225], v[184:191], v[100:103]
	v_mfma_f32_16x16x128_f8f6f4 v[96:99], v[226:233], v[184:191], v[96:99]
	v_mfma_f32_16x16x128_f8f6f4 v[84:87], v[218:225], v[196:203], v[84:87]
	v_mfma_f32_16x16x128_f8f6f4 v[80:83], v[226:233], v[196:203], v[80:83]
	v_mfma_f32_16x16x128_f8f6f4 v[68:71], v[218:225], v[204:211], v[68:71]
	v_mfma_f32_16x16x128_f8f6f4 v[64:67], v[226:233], v[204:211], v[64:67]
	s_setprio 0
	s_barrier
	s_mov_b32 m0, s1
	ds_read_b128 v[176:179], v145 offset:16384
	ds_read_b128 v[184:187], v145 offset:18432
	ds_read_b128 v[180:183], v146 offset:16384
	ds_read_b128 v[188:191], v146 offset:18432
	ds_read_b128 v[196:199], v145 offset:20480
	ds_read_b128 v[204:207], v145 offset:22528
	ds_read_b128 v[200:203], v146 offset:20480
	ds_read_b128 v[208:211], v146 offset:22528
	global_load_lds_dwordx4 v132, s[36:37]
	s_mov_b32 m0, s48
	v_mov_b32_e32 v141, v133
	global_load_lds_dwordx4 v140, s[36:37]
	s_barrier
	s_waitcnt lgkmcnt(0)
	v_lshl_add_u64 v[192:193], s[36:37], 0, v[132:133]
	v_lshl_add_u64 v[212:213], s[36:37], 0, v[140:141]
	s_setprio 1
	s_waitcnt lgkmcnt(0)
	v_mfma_f32_16x16x128_f8f6f4 v[60:63], v[160:167], v[176:183], v[60:63]
	v_mfma_f32_16x16x128_f8f6f4 v[56:59], v[168:175], v[176:183], v[56:59]
	v_mfma_f32_16x16x128_f8f6f4 v[44:47], v[160:167], v[184:191], v[44:47]
	v_mfma_f32_16x16x128_f8f6f4 v[40:43], v[168:175], v[184:191], v[40:43]
	v_mfma_f32_16x16x128_f8f6f4 v[28:31], v[160:167], v[196:203], v[28:31]
	v_mfma_f32_16x16x128_f8f6f4 v[24:27], v[168:175], v[196:203], v[24:27]
	v_mfma_f32_16x16x128_f8f6f4 v[12:15], v[160:167], v[204:211], v[12:15]
	v_mfma_f32_16x16x128_f8f6f4 v[8:11], v[168:175], v[204:211], v[8:11]
	s_setprio 0
	s_barrier
	s_mov_b32 m0, s46
	v_lshl_add_u64 v[140:141], s[40:41], 0, v[130:131]
	global_load_lds_dwordx4 v[140:141], off
	v_lshl_add_u64 v[142:143], s[40:41], 0, v[128:129]
	s_mov_b32 m0, s47
	s_nop 0
	global_load_lds_dwordx4 v[142:143], off
	s_waitcnt vmcnt(8)
	s_barrier
	s_setprio 1
	s_waitcnt lgkmcnt(0)
	v_mfma_f32_16x16x128_f8f6f4 v[52:55], v[218:225], v[176:183], v[52:55]
	v_mfma_f32_16x16x128_f8f6f4 v[48:51], v[226:233], v[176:183], v[48:51]
	v_mfma_f32_16x16x128_f8f6f4 v[36:39], v[218:225], v[184:191], v[36:39]
	v_mfma_f32_16x16x128_f8f6f4 v[32:35], v[226:233], v[184:191], v[32:35]
	v_mfma_f32_16x16x128_f8f6f4 v[20:23], v[218:225], v[196:203], v[20:23]
	v_mfma_f32_16x16x128_f8f6f4 v[16:19], v[226:233], v[196:203], v[16:19]
	v_mfma_f32_16x16x128_f8f6f4 v[4:7], v[218:225], v[204:211], v[4:7]
	v_mfma_f32_16x16x128_f8f6f4 v[0:3], v[226:233], v[204:211], v[0:3]
	s_setprio 0
	s_barrier
	ds_read_b128 v[160:163], v147 offset:32768
	ds_read_b128 v[168:171], v147 offset:34816
	ds_read_b128 v[164:167], v148 offset:32768
	ds_read_b128 v[172:175], v148 offset:34816
	s_mov_b32 m0, s51
	ds_read_b128 v[176:179], v145 offset:32768
	ds_read_b128 v[184:187], v145 offset:34816
	ds_read_b128 v[180:183], v146 offset:32768
	ds_read_b128 v[188:191], v146 offset:34816
	ds_read_b128 v[196:199], v145 offset:36864
	ds_read_b128 v[204:207], v145 offset:38912
	ds_read_b128 v[200:203], v146 offset:36864
	ds_read_b128 v[208:211], v146 offset:38912
	v_cndmask_b32_e64 v132, v138, v158, s[30:31]
	global_load_lds_dwordx4 v159, s[36:37]
	s_mov_b32 m0, s52
	s_nop 0
	global_load_lds_dwordx4 v132, s[36:37]
	s_waitcnt vmcnt(8)
	s_waitcnt lgkmcnt(8)
	s_barrier
	s_waitcnt lgkmcnt(0)
	s_setprio 1
	v_mfma_f32_16x16x128_f8f6f4 v[124:127], v[160:167], v[176:183], v[124:127]
	v_mfma_f32_16x16x128_f8f6f4 v[120:123], v[168:175], v[176:183], v[120:123]
	v_mfma_f32_16x16x128_f8f6f4 v[108:111], v[160:167], v[184:191], v[108:111]
	v_mfma_f32_16x16x128_f8f6f4 v[104:107], v[168:175], v[184:191], v[104:107]
	v_mfma_f32_16x16x128_f8f6f4 v[92:95], v[160:167], v[196:203], v[92:95]
	v_mfma_f32_16x16x128_f8f6f4 v[88:91], v[168:175], v[196:203], v[88:91]
	v_mfma_f32_16x16x128_f8f6f4 v[76:79], v[160:167], v[204:211], v[76:79]
	v_mfma_f32_16x16x128_f8f6f4 v[72:75], v[168:175], v[204:211], v[72:75]
	s_setprio 0
	s_barrier
	ds_read_b128 v[218:221], v147 offset:49152
	ds_read_b128 v[226:229], v147 offset:51200
	ds_read_b128 v[222:225], v148 offset:49152
	ds_read_b128 v[230:233], v148 offset:51200
	v_lshl_add_u64 v[214:215], s[38:39], 0, v[130:131]
	s_mov_b32 m0, s49
	s_nop 0
	global_load_lds_dwordx4 v[214:215], off
	v_lshl_add_u64 v[214:215], s[38:39], 0, v[128:129]
	s_mov_b32 m0, s50
	s_nop 0
	global_load_lds_dwordx4 v[214:215], off
	s_waitcnt vmcnt(8)
	s_barrier
	s_waitcnt lgkmcnt(0)
	s_setprio 1
	v_mfma_f32_16x16x128_f8f6f4 v[116:119], v[218:225], v[176:183], v[116:119]
	v_mfma_f32_16x16x128_f8f6f4 v[112:115], v[226:233], v[176:183], v[112:115]
	v_mfma_f32_16x16x128_f8f6f4 v[100:103], v[218:225], v[184:191], v[100:103]
	v_mfma_f32_16x16x128_f8f6f4 v[96:99], v[226:233], v[184:191], v[96:99]
	v_mfma_f32_16x16x128_f8f6f4 v[84:87], v[218:225], v[196:203], v[84:87]
	v_mfma_f32_16x16x128_f8f6f4 v[80:83], v[226:233], v[196:203], v[80:83]
	v_mfma_f32_16x16x128_f8f6f4 v[68:71], v[218:225], v[204:211], v[68:71]
	v_mfma_f32_16x16x128_f8f6f4 v[64:67], v[226:233], v[204:211], v[64:67]
	s_setprio 0
	s_barrier
	s_mov_b32 m0, s56
	v_lshl_add_u64 v[192:193], v[192:193], 0, s[16:17]
	ds_read_b128 v[176:179], v145 offset:49152
	ds_read_b128 v[184:187], v145 offset:51200
	ds_read_b128 v[180:183], v146 offset:49152
	ds_read_b128 v[188:191], v146 offset:51200
	ds_read_b128 v[196:199], v145 offset:53248
	ds_read_b128 v[204:207], v145 offset:55296
	ds_read_b128 v[200:203], v146 offset:53248
	ds_read_b128 v[208:211], v146 offset:55296
	global_load_lds_dwordx4 v[192:193], off
	v_lshl_add_u64 v[192:193], v[212:213], 0, s[16:17]
	s_mov_b32 m0, s57
	s_nop 0
	global_load_lds_dwordx4 v[192:193], off
	s_barrier
	s_waitcnt lgkmcnt(0)
	s_setprio 1
	v_mfma_f32_16x16x128_f8f6f4 v[60:63], v[160:167], v[176:183], v[60:63]
	v_mfma_f32_16x16x128_f8f6f4 v[56:59], v[168:175], v[176:183], v[56:59]
	v_mfma_f32_16x16x128_f8f6f4 v[44:47], v[160:167], v[184:191], v[44:47]
	v_mfma_f32_16x16x128_f8f6f4 v[40:43], v[168:175], v[184:191], v[40:43]
	v_mfma_f32_16x16x128_f8f6f4 v[28:31], v[160:167], v[196:203], v[28:31]
	v_mfma_f32_16x16x128_f8f6f4 v[24:27], v[168:175], v[196:203], v[24:27]
	v_mfma_f32_16x16x128_f8f6f4 v[12:15], v[160:167], v[204:211], v[12:15]
	v_mfma_f32_16x16x128_f8f6f4 v[8:11], v[168:175], v[204:211], v[8:11]
	s_setprio 0
	s_barrier
	s_mov_b32 m0, s54
	v_lshl_add_u64 v[140:141], v[140:141], 0, s[16:17]
	global_load_lds_dwordx4 v[140:141], off
	v_lshl_add_u64 v[140:141], v[142:143], 0, s[16:17]
	s_mov_b32 m0, s55
	s_nop 0
	global_load_lds_dwordx4 v[140:141], off
	s_waitcnt vmcnt(8)
	s_barrier
	s_setprio 1
	s_waitcnt lgkmcnt(0)
	v_mfma_f32_16x16x128_f8f6f4 v[52:55], v[218:225], v[176:183], v[52:55]
	v_mfma_f32_16x16x128_f8f6f4 v[48:51], v[226:233], v[176:183], v[48:51]
	v_mfma_f32_16x16x128_f8f6f4 v[36:39], v[218:225], v[184:191], v[36:39]
	v_mfma_f32_16x16x128_f8f6f4 v[32:35], v[226:233], v[184:191], v[32:35]
	v_mfma_f32_16x16x128_f8f6f4 v[20:23], v[218:225], v[196:203], v[20:23]
	v_mfma_f32_16x16x128_f8f6f4 v[16:19], v[226:233], v[196:203], v[16:19]
	v_mfma_f32_16x16x128_f8f6f4 v[4:7], v[218:225], v[204:211], v[4:7]
	v_mfma_f32_16x16x128_f8f6f4 v[0:3], v[226:233], v[204:211], v[0:3]
	s_setprio 0
	s_barrier
	s_mov_b32 m0, s58
	v_lshl_add_u64 v[140:141], s[34:35], 0, v[130:131]
	global_load_lds_dwordx4 v[140:141], off
	v_lshl_add_u64 v[140:141], s[34:35], 0, v[128:129]
	s_mov_b32 m0, s59
	s_andn2_b64 vcc, exec, s[28:29]
	global_load_lds_dwordx4 v[140:141], off
	s_mov_b64 s[30:31], -1
	s_mov_b64 s[28:29], 0
	s_mov_b64 s[34:35], 0x100
	s_cbranch_vccz .LBB0_1081

.LBB0_1503:
	s_add_u32 s36, s8, s34
	s_addc_u32 s37, s9, s35
	s_add_u32 s38, s36, 0x6ea00100
	ds_read_b128 v[144:147], v168
	ds_read_b128 v[152:155], v168 offset:2048
	ds_read_b128 v[148:151], v169
	ds_read_b128 v[156:159], v169 offset:2048
	s_addc_u32 s39, s37, 0
	s_add_u32 s60, s56, s34
	s_addc_u32 s61, s57, s35
	s_cmpk_eq_i32 s34, 0x700
	s_cselect_b64 vcc, -1, 0
	s_and_b64 s[36:37], vcc, exec
	ds_read_b128 v[184:187], v166
	ds_read_b128 v[196:199], v166 offset:2048
	ds_read_b128 v[188:191], v167
	ds_read_b128 v[200:203], v167 offset:2048
	ds_read_b128 v[204:207], v166 offset:4096
	ds_read_b128 v[212:215], v166 offset:6144
	ds_read_b128 v[208:211], v167 offset:4096
	ds_read_b128 v[216:219], v167 offset:6144
	s_waitcnt vmcnt(6)
	s_waitcnt lgkmcnt(8)
	s_barrier
	s_waitcnt lgkmcnt(0)
	v_cndmask_b32_e32 v160, v134, v180, vcc
	s_setprio 1
	s_waitcnt lgkmcnt(0)
	v_mfma_f32_16x16x128_f8f6f4 v[124:127], v[144:151], v[184:191], v[124:127]
	v_mfma_f32_16x16x128_f8f6f4 v[120:123], v[152:159], v[184:191], v[120:123]
	v_mfma_f32_16x16x128_f8f6f4 v[112:115], v[144:151], v[196:203], v[112:115]
	v_mfma_f32_16x16x128_f8f6f4 v[104:107], v[152:159], v[196:203], v[104:107]
	v_mfma_f32_16x16x128_f8f6f4 v[96:99], v[144:151], v[204:211], v[96:99]
	v_mfma_f32_16x16x128_f8f6f4 v[88:91], v[152:159], v[204:211], v[88:91]
	v_mfma_f32_16x16x128_f8f6f4 v[80:83], v[144:151], v[212:219], v[80:83]
	v_mfma_f32_16x16x128_f8f6f4 v[72:75], v[152:159], v[212:219], v[72:75]
	s_setprio 0
	s_barrier
	ds_read_b128 v[228:231], v168 offset:16384
	ds_read_b128 v[236:239], v168 offset:18432
	ds_read_b128 v[232:235], v169 offset:16384
	ds_read_b128 v[240:243], v169 offset:18432
	v_cndmask_b32_e32 v132, v135, v179, vcc
	s_cselect_b32 s39, s11, s39
	s_cselect_b32 s38, s10, s38
	s_cselect_b32 s37, s31, s61
	s_cselect_b32 s36, s30, s60
	v_cndmask_b32_e32 v137, v136, v181, vcc
	v_lshl_add_u64 v[252:253], v[142:143], 0, s[34:35]
	s_add_i32 m0, s27, 0xc000
	s_nop 0
	global_load_lds_dwordx4 v[252:253], off
	v_lshl_add_u64 v[252:253], v[140:141], 0, s[34:35]
	s_add_i32 m0, s27, 0xe000
	s_nop 0
	global_load_lds_dwordx4 v[252:253], off
	s_barrier
	s_waitcnt lgkmcnt(0)
	s_setprio 1
	v_mfma_f32_16x16x128_f8f6f4 v[116:119], v[228:235], v[184:191], v[116:119]
	v_mfma_f32_16x16x128_f8f6f4 v[108:111], v[236:243], v[184:191], v[108:111]
	v_mfma_f32_16x16x128_f8f6f4 v[100:103], v[228:235], v[196:203], v[100:103]
	v_mfma_f32_16x16x128_f8f6f4 v[92:95], v[236:243], v[196:203], v[92:95]
	v_mfma_f32_16x16x128_f8f6f4 v[84:87], v[228:235], v[204:211], v[84:87]
	v_mfma_f32_16x16x128_f8f6f4 v[76:79], v[236:243], v[204:211], v[76:79]
	v_mfma_f32_16x16x128_f8f6f4 v[68:71], v[228:235], v[212:219], v[68:71]
	v_mfma_f32_16x16x128_f8f6f4 v[64:67], v[236:243], v[212:219], v[64:67]
	s_setprio 0
	s_barrier
	s_mov_b32 m0, s27
	ds_read_b128 v[196:199], v166 offset:16384
	ds_read_b128 v[204:207], v166 offset:18432
	ds_read_b128 v[200:203], v167 offset:16384
	ds_read_b128 v[208:211], v167 offset:18432
	ds_read_b128 v[212:215], v166 offset:20480
	ds_read_b128 v[220:223], v166 offset:22528
	ds_read_b128 v[216:219], v167 offset:20480
	ds_read_b128 v[224:227], v167 offset:22528
	global_load_lds_dwordx4 v132, s[38:39]
	s_mov_b32 m0, s41
	v_mov_b32_e32 v161, v133
	global_load_lds_dwordx4 v160, s[38:39]
	s_barrier
	s_waitcnt lgkmcnt(0)
	v_lshl_add_u64 v[246:247], s[38:39], 0, v[132:133]
	v_lshl_add_u64 v[244:245], s[38:39], 0, v[160:161]
	s_setprio 1
	s_waitcnt lgkmcnt(0)
	v_mfma_f32_16x16x128_f8f6f4 v[60:63], v[144:151], v[196:203], v[60:63]
	v_mfma_f32_16x16x128_f8f6f4 v[56:59], v[152:159], v[196:203], v[56:59]
	v_mfma_f32_16x16x128_f8f6f4 v[48:51], v[144:151], v[204:211], v[48:51]
	v_mfma_f32_16x16x128_f8f6f4 v[40:43], v[152:159], v[204:211], v[40:43]
	v_mfma_f32_16x16x128_f8f6f4 v[32:35], v[144:151], v[212:219], v[32:35]
	v_mfma_f32_16x16x128_f8f6f4 v[24:27], v[152:159], v[212:219], v[24:27]
	v_mfma_f32_16x16x128_f8f6f4 v[16:19], v[144:151], v[220:227], v[16:19]
	v_mfma_f32_16x16x128_f8f6f4 v[8:11], v[152:159], v[220:227], v[8:11]
	s_setprio 0
	s_barrier
	s_mov_b32 m0, s33
	v_lshl_add_u64 v[144:145], s[36:37], 0, v[128:129]
	global_load_lds_dwordx4 v[144:145], off
	v_lshl_add_u64 v[146:147], s[36:37], 0, v[130:131]
	s_mov_b32 m0, s40
	s_nop 0
	global_load_lds_dwordx4 v[146:147], off
	s_waitcnt vmcnt(8)
	s_barrier
	s_setprio 1
	s_waitcnt lgkmcnt(0)
	v_mfma_f32_16x16x128_f8f6f4 v[52:55], v[228:235], v[196:203], v[52:55]
	v_mfma_f32_16x16x128_f8f6f4 v[44:47], v[236:243], v[196:203], v[44:47]
	v_mfma_f32_16x16x128_f8f6f4 v[36:39], v[228:235], v[204:211], v[36:39]
	v_mfma_f32_16x16x128_f8f6f4 v[28:31], v[236:243], v[204:211], v[28:31]
	v_mfma_f32_16x16x128_f8f6f4 v[20:23], v[228:235], v[212:219], v[20:23]
	v_mfma_f32_16x16x128_f8f6f4 v[12:15], v[236:243], v[212:219], v[12:15]
	v_mfma_f32_16x16x128_f8f6f4 v[4:7], v[228:235], v[220:227], v[4:7]
	v_mfma_f32_16x16x128_f8f6f4 v[0:3], v[236:243], v[220:227], v[0:3]
	s_setprio 0
	s_barrier
	ds_read_b128 v[152:155], v168 offset:32768
	ds_read_b128 v[184:187], v168 offset:34816
	ds_read_b128 v[156:159], v169 offset:32768
	ds_read_b128 v[188:191], v169 offset:34816
	s_mov_b32 m0, s44
	ds_read_b128 v[196:199], v166 offset:32768
	ds_read_b128 v[204:207], v166 offset:34816
	ds_read_b128 v[200:203], v167 offset:32768
	ds_read_b128 v[208:211], v167 offset:34816
	ds_read_b128 v[212:215], v166 offset:36864
	ds_read_b128 v[220:223], v166 offset:38912
	ds_read_b128 v[216:219], v167 offset:36864
	ds_read_b128 v[224:227], v167 offset:38912
	v_cndmask_b32_e32 v132, v138, v182, vcc
	global_load_lds_dwordx4 v137, s[38:39]
	s_mov_b32 m0, s45
	s_nop 0
	global_load_lds_dwordx4 v132, s[38:39]
	s_waitcnt vmcnt(8)
	s_waitcnt lgkmcnt(8)
	s_barrier
	s_waitcnt lgkmcnt(0)
	s_setprio 1
	v_mfma_f32_16x16x128_f8f6f4 v[124:127], v[152:159], v[196:203], v[124:127]
	v_mfma_f32_16x16x128_f8f6f4 v[120:123], v[184:191], v[196:203], v[120:123]
	v_mfma_f32_16x16x128_f8f6f4 v[112:115], v[152:159], v[204:211], v[112:115]
	v_mfma_f32_16x16x128_f8f6f4 v[104:107], v[184:191], v[204:211], v[104:107]
	v_mfma_f32_16x16x128_f8f6f4 v[96:99], v[152:159], v[212:219], v[96:99]
	v_mfma_f32_16x16x128_f8f6f4 v[88:91], v[184:191], v[212:219], v[88:91]
	v_mfma_f32_16x16x128_f8f6f4 v[80:83], v[152:159], v[220:227], v[80:83]
	v_mfma_f32_16x16x128_f8f6f4 v[72:75], v[184:191], v[220:227], v[72:75]
	s_setprio 0
	s_barrier
	ds_read_b128 v[228:231], v168 offset:49152
	ds_read_b128 v[236:239], v168 offset:51200
	ds_read_b128 v[232:235], v169 offset:49152
	ds_read_b128 v[240:243], v169 offset:51200
	s_add_u32 s38, s36, 0x40000
	s_addc_u32 s39, s37, 0
	v_lshl_add_u64 v[160:161], s[38:39], 0, v[128:129]
	s_mov_b32 m0, s42
	s_nop 0
	global_load_lds_dwordx4 v[160:161], off
	v_lshl_add_u64 v[160:161], s[38:39], 0, v[130:131]
	s_mov_b32 m0, s43
	s_nop 0
	global_load_lds_dwordx4 v[160:161], off
	s_waitcnt vmcnt(8)
	s_barrier
	s_waitcnt lgkmcnt(0)
	s_setprio 1
	v_mfma_f32_16x16x128_f8f6f4 v[116:119], v[228:235], v[196:203], v[116:119]
	v_mfma_f32_16x16x128_f8f6f4 v[108:111], v[236:243], v[196:203], v[108:111]
	v_mfma_f32_16x16x128_f8f6f4 v[100:103], v[228:235], v[204:211], v[100:103]
	v_mfma_f32_16x16x128_f8f6f4 v[92:95], v[236:243], v[204:211], v[92:95]
	v_mfma_f32_16x16x128_f8f6f4 v[84:87], v[228:235], v[212:219], v[84:87]
	v_mfma_f32_16x16x128_f8f6f4 v[76:79], v[236:243], v[212:219], v[76:79]
	v_mfma_f32_16x16x128_f8f6f4 v[68:71], v[228:235], v[220:227], v[68:71]
	v_mfma_f32_16x16x128_f8f6f4 v[64:67], v[236:243], v[220:227], v[64:67]
	s_setprio 0
	s_barrier
	s_mov_b32 m0, s50
	v_lshl_add_u64 v[246:247], v[246:247], 0, s[16:17]
	ds_read_b128 v[196:199], v166 offset:49152
	ds_read_b128 v[204:207], v166 offset:51200
	ds_read_b128 v[200:203], v167 offset:49152
	ds_read_b128 v[208:211], v167 offset:51200
	ds_read_b128 v[212:215], v166 offset:53248
	ds_read_b128 v[220:223], v166 offset:55296
	ds_read_b128 v[216:219], v167 offset:53248
	ds_read_b128 v[224:227], v167 offset:55296
	global_load_lds_dwordx4 v[246:247], off
	v_lshl_add_u64 v[244:245], v[244:245], 0, s[16:17]
	s_mov_b32 m0, s51
	s_nop 0
	global_load_lds_dwordx4 v[244:245], off
	s_barrier
	s_waitcnt lgkmcnt(0)
	s_setprio 1
	v_mfma_f32_16x16x128_f8f6f4 v[60:63], v[152:159], v[196:203], v[60:63]
	v_mfma_f32_16x16x128_f8f6f4 v[56:59], v[184:191], v[196:203], v[56:59]
	v_mfma_f32_16x16x128_f8f6f4 v[48:51], v[152:159], v[204:211], v[48:51]
	v_mfma_f32_16x16x128_f8f6f4 v[40:43], v[184:191], v[204:211], v[40:43]
	v_mfma_f32_16x16x128_f8f6f4 v[32:35], v[152:159], v[212:219], v[32:35]
	v_mfma_f32_16x16x128_f8f6f4 v[24:27], v[184:191], v[212:219], v[24:27]
	v_mfma_f32_16x16x128_f8f6f4 v[16:19], v[152:159], v[220:227], v[16:19]
	v_mfma_f32_16x16x128_f8f6f4 v[8:11], v[184:191], v[220:227], v[8:11]
	s_setprio 0
	s_barrier
	s_mov_b32 m0, s48
	v_lshl_add_u64 v[144:145], v[144:145], 0, s[16:17]
	global_load_lds_dwordx4 v[144:145], off
	v_lshl_add_u64 v[144:145], v[146:147], 0, s[16:17]
	s_mov_b32 m0, s49
	s_nop 0
	global_load_lds_dwordx4 v[144:145], off
	s_waitcnt vmcnt(8)
	s_barrier
	s_setprio 1
	s_waitcnt lgkmcnt(0)
	v_mfma_f32_16x16x128_f8f6f4 v[52:55], v[228:235], v[196:203], v[52:55]
	v_mfma_f32_16x16x128_f8f6f4 v[44:47], v[236:243], v[196:203], v[44:47]
	v_mfma_f32_16x16x128_f8f6f4 v[36:39], v[228:235], v[204:211], v[36:39]
	v_mfma_f32_16x16x128_f8f6f4 v[28:31], v[236:243], v[204:211], v[28:31]
	v_mfma_f32_16x16x128_f8f6f4 v[20:23], v[228:235], v[212:219], v[20:23]
	v_mfma_f32_16x16x128_f8f6f4 v[12:15], v[236:243], v[212:219], v[12:15]
	v_mfma_f32_16x16x128_f8f6f4 v[4:7], v[228:235], v[220:227], v[4:7]
	v_mfma_f32_16x16x128_f8f6f4 v[0:3], v[236:243], v[220:227], v[0:3]
	s_setprio 0
	s_barrier
	s_add_u32 s36, s36, 0x40080
	s_addc_u32 s37, s37, 0
	s_mov_b32 m0, s52
	v_lshl_add_u64 v[144:145], s[36:37], 0, v[128:129]
	global_load_lds_dwordx4 v[144:145], off
	v_lshl_add_u64 v[144:145], s[36:37], 0, v[130:131]
	s_mov_b32 m0, s53
	s_add_i32 s59, s59, 2
	global_load_lds_dwordx4 v[144:145], off
	s_add_u32 s34, s34, 0x100
	s_addc_u32 s35, s35, 0
	s_cmp_gt_u32 s59, 13
	s_cbranch_scc0 .LBB0_1503
	s_and_b64 vcc, exec, s[20:21]
	s_cbranch_vccz .LBB0_1506
	s_barrier

.LBB0_1960:
	v_mov_b32_e32 v137, v133
	v_mov_b32_e32 v139, v133
	s_mov_b64 s[44:45], 0
	s_mov_b64 s[40:41], -1
	s_mov_b64 s[42:43], 0
	s_add_u32 s52, s12, s44
	s_addc_u32 s53, s13, s45
	s_add_u32 s29, s52, 0x100
	s_addc_u32 s48, s53, 0
	s_and_b64 s[46:47], s[42:43], exec
	s_cselect_b32 s46, s12, s29
	s_cselect_b32 s47, s13, s48
	s_add_u32 s29, s38, s44
	s_addc_u32 s44, s39, s45
	s_add_u32 s29, s29, 0x100
	s_addc_u32 s48, s44, 0
	ds_read_b128 v[162:165], v147
	ds_read_b128 v[170:173], v147 offset:2048
	ds_read_b128 v[166:169], v148
	ds_read_b128 v[174:177], v148 offset:2048
	s_and_b64 s[44:45], s[42:43], exec
	s_cselect_b32 s51, s35, s48
	s_cselect_b32 s50, s34, s29
	ds_read_b128 v[178:181], v145
	ds_read_b128 v[186:189], v145 offset:2048
	ds_read_b128 v[182:185], v146
	ds_read_b128 v[190:193], v146 offset:2048
	ds_read_b128 v[196:199], v145 offset:4096
	ds_read_b128 v[204:207], v145 offset:6144
	ds_read_b128 v[200:203], v146 offset:4096
	ds_read_b128 v[208:211], v146 offset:6144
	s_waitcnt vmcnt(6)
	s_waitcnt lgkmcnt(8)
	s_barrier
	s_waitcnt lgkmcnt(0)
	v_cndmask_b32_e64 v140, v134, v158, s[42:43]
	s_setprio 1
	s_waitcnt lgkmcnt(0)
	v_mfma_f32_16x16x128_f8f6f4 v[124:127], v[162:169], v[178:185], 0
	v_mfma_f32_16x16x128_f8f6f4 v[120:123], v[170:177], v[178:185], 0
	v_mfma_f32_16x16x128_f8f6f4 v[108:111], v[162:169], v[186:193], 0
	v_mfma_f32_16x16x128_f8f6f4 v[104:107], v[170:177], v[186:193], 0
	v_mfma_f32_16x16x128_f8f6f4 v[92:95], v[162:169], v[196:203], 0
	v_mfma_f32_16x16x128_f8f6f4 v[88:91], v[170:177], v[196:203], 0
	v_mfma_f32_16x16x128_f8f6f4 v[76:79], v[162:169], v[204:211], 0
	v_mfma_f32_16x16x128_f8f6f4 v[72:75], v[170:177], v[204:211], 0
	s_setprio 0
	s_barrier
	ds_read_b128 v[218:221], v147 offset:16384
	ds_read_b128 v[226:229], v147 offset:18432
	ds_read_b128 v[222:225], v148 offset:16384
	ds_read_b128 v[230:233], v148 offset:18432
	s_add_i32 m0, s0, 0xc000
	s_add_i32 s29, s0, 0xe000
	s_add_u32 s48, s50, 0x1000
	s_addc_u32 s49, s51, 0
	s_add_u32 s44, s50, 0x1080
	s_addc_u32 s45, s51, 0
	v_cndmask_b32_e64 v132, v135, v157, s[42:43]
	v_cndmask_b32_e64 v161, v136, v159, s[42:43]
	v_lshl_add_u64 v[252:253], s[52:53], 0, v[136:137]
	v_lshl_add_u64 v[252:253], v[252:253], 0, s[20:21]
	global_load_lds_dwordx4 v[252:253], off
	v_lshl_add_u64 v[252:253], s[52:53], 0, v[138:139]
	v_lshl_add_u64 v[252:253], v[252:253], 0, s[20:21]
	s_mov_b32 m0, s29
	s_nop 0
	global_load_lds_dwordx4 v[252:253], off
	s_barrier
	s_waitcnt lgkmcnt(0)
	s_setprio 1
	v_mfma_f32_16x16x128_f8f6f4 v[116:119], v[218:225], v[178:185], 0
	v_mfma_f32_16x16x128_f8f6f4 v[112:115], v[226:233], v[178:185], 0
	v_mfma_f32_16x16x128_f8f6f4 v[100:103], v[218:225], v[186:193], 0
	v_mfma_f32_16x16x128_f8f6f4 v[96:99], v[226:233], v[186:193], 0
	v_mfma_f32_16x16x128_f8f6f4 v[84:87], v[218:225], v[196:203], 0
	v_mfma_f32_16x16x128_f8f6f4 v[80:83], v[226:233], v[196:203], 0
	v_mfma_f32_16x16x128_f8f6f4 v[68:71], v[218:225], v[204:211], 0
	v_mfma_f32_16x16x128_f8f6f4 v[64:67], v[226:233], v[204:211], 0
	s_setprio 0
	s_barrier
	s_mov_b32 m0, s0
	ds_read_b128 v[178:181], v145 offset:16384
	ds_read_b128 v[186:189], v145 offset:18432
	ds_read_b128 v[182:185], v146 offset:16384
	ds_read_b128 v[190:193], v146 offset:18432
	ds_read_b128 v[196:199], v145 offset:20480
	ds_read_b128 v[204:207], v145 offset:22528
	ds_read_b128 v[200:203], v146 offset:20480
	ds_read_b128 v[208:211], v146 offset:22528
	global_load_lds_dwordx4 v132, s[46:47]
	s_mov_b32 m0, s56
	v_mov_b32_e32 v141, v133
	global_load_lds_dwordx4 v140, s[46:47]
	s_barrier
	s_waitcnt lgkmcnt(0)
	v_lshl_add_u64 v[212:213], s[46:47], 0, v[132:133]
	v_lshl_add_u64 v[214:215], s[46:47], 0, v[140:141]
	s_setprio 1
	s_waitcnt lgkmcnt(0)
	v_mfma_f32_16x16x128_f8f6f4 v[60:63], v[162:169], v[178:185], 0
	v_mfma_f32_16x16x128_f8f6f4 v[56:59], v[170:177], v[178:185], 0
	v_mfma_f32_16x16x128_f8f6f4 v[44:47], v[162:169], v[186:193], 0
	v_mfma_f32_16x16x128_f8f6f4 v[40:43], v[170:177], v[186:193], 0
	v_mfma_f32_16x16x128_f8f6f4 v[28:31], v[162:169], v[196:203], 0
	v_mfma_f32_16x16x128_f8f6f4 v[24:27], v[170:177], v[196:203], 0
	v_mfma_f32_16x16x128_f8f6f4 v[12:15], v[162:169], v[204:211], 0
	v_mfma_f32_16x16x128_f8f6f4 v[8:11], v[170:177], v[204:211], 0
	s_setprio 0
	s_barrier
	s_mov_b32 m0, s1
	v_lshl_add_u64 v[140:141], s[50:51], 0, v[128:129]
	global_load_lds_dwordx4 v[140:141], off
	v_lshl_add_u64 v[142:143], s[50:51], 0, v[130:131]
	s_mov_b32 m0, s37
	s_nop 0
	global_load_lds_dwordx4 v[142:143], off
	s_waitcnt vmcnt(8)
	s_barrier
	s_setprio 1
	s_waitcnt lgkmcnt(0)
	v_mfma_f32_16x16x128_f8f6f4 v[52:55], v[218:225], v[178:185], 0
	v_mfma_f32_16x16x128_f8f6f4 v[48:51], v[226:233], v[178:185], 0
	v_mfma_f32_16x16x128_f8f6f4 v[36:39], v[218:225], v[186:193], 0
	v_mfma_f32_16x16x128_f8f6f4 v[32:35], v[226:233], v[186:193], 0
	v_mfma_f32_16x16x128_f8f6f4 v[20:23], v[218:225], v[196:203], 0
	v_mfma_f32_16x16x128_f8f6f4 v[16:19], v[226:233], v[196:203], 0
	v_mfma_f32_16x16x128_f8f6f4 v[4:7], v[218:225], v[204:211], 0
	v_mfma_f32_16x16x128_f8f6f4 v[0:3], v[226:233], v[204:211], 0
	s_setprio 0
	s_barrier
	ds_read_b128 v[162:165], v147 offset:32768
	ds_read_b128 v[170:173], v147 offset:34816
	ds_read_b128 v[166:169], v148 offset:32768
	ds_read_b128 v[174:177], v148 offset:34816
	s_mov_b32 m0, s65
	ds_read_b128 v[178:181], v145 offset:32768
	ds_read_b128 v[186:189], v145 offset:34816
	ds_read_b128 v[182:185], v146 offset:32768
	ds_read_b128 v[190:193], v146 offset:34816
	ds_read_b128 v[196:199], v145 offset:36864
	ds_read_b128 v[204:207], v145 offset:38912
	ds_read_b128 v[200:203], v146 offset:36864
	ds_read_b128 v[208:211], v146 offset:38912
	v_cndmask_b32_e64 v132, v138, v160, s[42:43]
	global_load_lds_dwordx4 v161, s[46:47]
	s_mov_b32 m0, s66
	s_nop 0
	global_load_lds_dwordx4 v132, s[46:47]
	s_waitcnt vmcnt(8)
	s_waitcnt lgkmcnt(8)
	s_barrier
	s_waitcnt lgkmcnt(0)
	s_setprio 1
	v_mfma_f32_16x16x128_f8f6f4 v[124:127], v[162:169], v[178:185], v[124:127]
	v_mfma_f32_16x16x128_f8f6f4 v[120:123], v[170:177], v[178:185], v[120:123]
	v_mfma_f32_16x16x128_f8f6f4 v[108:111], v[162:169], v[186:193], v[108:111]
	v_mfma_f32_16x16x128_f8f6f4 v[104:107], v[170:177], v[186:193], v[104:107]
	v_mfma_f32_16x16x128_f8f6f4 v[92:95], v[162:169], v[196:203], v[92:95]
	v_mfma_f32_16x16x128_f8f6f4 v[88:91], v[170:177], v[196:203], v[88:91]
	v_mfma_f32_16x16x128_f8f6f4 v[76:79], v[162:169], v[204:211], v[76:79]
	v_mfma_f32_16x16x128_f8f6f4 v[72:75], v[170:177], v[204:211], v[72:75]
	s_setprio 0
	s_barrier
	ds_read_b128 v[218:221], v147 offset:49152
	ds_read_b128 v[226:229], v147 offset:51200
	ds_read_b128 v[222:225], v148 offset:49152
	ds_read_b128 v[230:233], v148 offset:51200
	v_lshl_add_u64 v[216:217], s[48:49], 0, v[128:129]
	s_mov_b32 m0, s57
	s_nop 0
	global_load_lds_dwordx4 v[216:217], off
	v_lshl_add_u64 v[216:217], s[48:49], 0, v[130:131]
	s_mov_b32 m0, s64
	s_nop 0
	global_load_lds_dwordx4 v[216:217], off
	s_waitcnt vmcnt(8)
	s_barrier
	s_waitcnt lgkmcnt(0)
	s_setprio 1
	v_mfma_f32_16x16x128_f8f6f4 v[116:119], v[218:225], v[178:185], v[116:119]
	v_mfma_f32_16x16x128_f8f6f4 v[112:115], v[226:233], v[178:185], v[112:115]
	v_mfma_f32_16x16x128_f8f6f4 v[100:103], v[218:225], v[186:193], v[100:103]
	v_mfma_f32_16x16x128_f8f6f4 v[96:99], v[226:233], v[186:193], v[96:99]
	v_mfma_f32_16x16x128_f8f6f4 v[84:87], v[218:225], v[196:203], v[84:87]
	v_mfma_f32_16x16x128_f8f6f4 v[80:83], v[226:233], v[196:203], v[80:83]
	v_mfma_f32_16x16x128_f8f6f4 v[68:71], v[218:225], v[204:211], v[68:71]
	v_mfma_f32_16x16x128_f8f6f4 v[64:67], v[226:233], v[204:211], v[64:67]
	s_setprio 0
	s_barrier
	s_mov_b32 m0, s69
	v_lshl_add_u64 v[212:213], v[212:213], 0, s[20:21]
	ds_read_b128 v[178:181], v145 offset:49152
	ds_read_b128 v[186:189], v145 offset:51200
	ds_read_b128 v[182:185], v146 offset:49152
	ds_read_b128 v[190:193], v146 offset:51200
	ds_read_b128 v[196:199], v145 offset:53248
	ds_read_b128 v[204:207], v145 offset:55296
	ds_read_b128 v[200:203], v146 offset:53248
	ds_read_b128 v[208:211], v146 offset:55296
	global_load_lds_dwordx4 v[212:213], off
	v_lshl_add_u64 v[212:213], v[214:215], 0, s[20:21]
	s_mov_b32 m0, s70
	s_nop 0
	global_load_lds_dwordx4 v[212:213], off
	s_barrier
	s_waitcnt lgkmcnt(0)
	s_setprio 1
	v_mfma_f32_16x16x128_f8f6f4 v[60:63], v[162:169], v[178:185], v[60:63]
	v_mfma_f32_16x16x128_f8f6f4 v[56:59], v[170:177], v[178:185], v[56:59]
	v_mfma_f32_16x16x128_f8f6f4 v[44:47], v[162:169], v[186:193], v[44:47]
	v_mfma_f32_16x16x128_f8f6f4 v[40:43], v[170:177], v[186:193], v[40:43]
	v_mfma_f32_16x16x128_f8f6f4 v[28:31], v[162:169], v[196:203], v[28:31]
	v_mfma_f32_16x16x128_f8f6f4 v[24:27], v[170:177], v[196:203], v[24:27]
	v_mfma_f32_16x16x128_f8f6f4 v[12:15], v[162:169], v[204:211], v[12:15]
	v_mfma_f32_16x16x128_f8f6f4 v[8:11], v[170:177], v[204:211], v[8:11]
	s_setprio 0
	s_barrier
	s_mov_b32 m0, s67
	v_lshl_add_u64 v[140:141], v[140:141], 0, s[20:21]
	global_load_lds_dwordx4 v[140:141], off
	v_lshl_add_u64 v[140:141], v[142:143], 0, s[20:21]
	s_mov_b32 m0, s68
	s_nop 0
	global_load_lds_dwordx4 v[140:141], off
	s_waitcnt vmcnt(8)
	s_barrier
	s_setprio 1
	s_waitcnt lgkmcnt(0)
	v_mfma_f32_16x16x128_f8f6f4 v[52:55], v[218:225], v[178:185], v[52:55]
	v_mfma_f32_16x16x128_f8f6f4 v[48:51], v[226:233], v[178:185], v[48:51]
	v_mfma_f32_16x16x128_f8f6f4 v[36:39], v[218:225], v[186:193], v[36:39]
	v_mfma_f32_16x16x128_f8f6f4 v[32:35], v[226:233], v[186:193], v[32:35]
	v_mfma_f32_16x16x128_f8f6f4 v[20:23], v[218:225], v[196:203], v[20:23]
	v_mfma_f32_16x16x128_f8f6f4 v[16:19], v[226:233], v[196:203], v[16:19]
	v_mfma_f32_16x16x128_f8f6f4 v[4:7], v[218:225], v[204:211], v[4:7]
	v_mfma_f32_16x16x128_f8f6f4 v[0:3], v[226:233], v[204:211], v[0:3]
	s_setprio 0
	s_barrier
	s_mov_b32 m0, s71
	v_lshl_add_u64 v[140:141], s[44:45], 0, v[128:129]
	global_load_lds_dwordx4 v[140:141], off
	v_lshl_add_u64 v[140:141], s[44:45], 0, v[130:131]
	s_mov_b32 m0, s72
	s_andn2_b64 vcc, exec, s[40:41]
	global_load_lds_dwordx4 v[140:141], off
	s_mov_b64 s[42:43], -1
	s_mov_b64 s[40:41], 0
	s_mov_b64 s[44:45], 0x100
	s_cbranch_vccz .LBB0_1961
	s_branch .Lpeel_after_1961
.LBB0_1961:
	s_add_u32 s52, s12, s44
	s_addc_u32 s53, s13, s45
	s_add_u32 s29, s52, 0x100
	s_addc_u32 s48, s53, 0
	s_and_b64 s[46:47], s[42:43], exec
	s_cselect_b32 s46, s12, s29
	s_cselect_b32 s47, s13, s48
	s_add_u32 s29, s38, s44
	s_addc_u32 s44, s39, s45
	s_add_u32 s29, s29, 0x100
	s_addc_u32 s48, s44, 0
	ds_read_b128 v[162:165], v147
	ds_read_b128 v[170:173], v147 offset:2048
	ds_read_b128 v[166:169], v148
	ds_read_b128 v[174:177], v148 offset:2048
	s_and_b64 s[44:45], s[42:43], exec
	s_cselect_b32 s51, s35, s48
	s_cselect_b32 s50, s34, s29
	ds_read_b128 v[178:181], v145
	ds_read_b128 v[186:189], v145 offset:2048
	ds_read_b128 v[182:185], v146
	ds_read_b128 v[190:193], v146 offset:2048
	ds_read_b128 v[196:199], v145 offset:4096
	ds_read_b128 v[204:207], v145 offset:6144
	ds_read_b128 v[200:203], v146 offset:4096
	ds_read_b128 v[208:211], v146 offset:6144
	s_waitcnt vmcnt(6)
	s_waitcnt lgkmcnt(8)
	s_barrier
	s_waitcnt lgkmcnt(0)
	v_cndmask_b32_e64 v140, v134, v158, s[42:43]
	s_setprio 1
	s_waitcnt lgkmcnt(0)
	v_mfma_f32_16x16x128_f8f6f4 v[124:127], v[162:169], v[178:185], v[124:127]
	v_mfma_f32_16x16x128_f8f6f4 v[120:123], v[170:177], v[178:185], v[120:123]
	v_mfma_f32_16x16x128_f8f6f4 v[108:111], v[162:169], v[186:193], v[108:111]
	v_mfma_f32_16x16x128_f8f6f4 v[104:107], v[170:177], v[186:193], v[104:107]
	v_mfma_f32_16x16x128_f8f6f4 v[92:95], v[162:169], v[196:203], v[92:95]
	v_mfma_f32_16x16x128_f8f6f4 v[88:91], v[170:177], v[196:203], v[88:91]
	v_mfma_f32_16x16x128_f8f6f4 v[76:79], v[162:169], v[204:211], v[76:79]
	v_mfma_f32_16x16x128_f8f6f4 v[72:75], v[170:177], v[204:211], v[72:75]
	s_setprio 0
	s_barrier
	ds_read_b128 v[218:221], v147 offset:16384
	ds_read_b128 v[226:229], v147 offset:18432
	ds_read_b128 v[222:225], v148 offset:16384
	ds_read_b128 v[230:233], v148 offset:18432
	s_add_i32 m0, s0, 0xc000
	s_add_i32 s29, s0, 0xe000
	s_add_u32 s48, s50, 0x1000
	s_addc_u32 s49, s51, 0
	s_add_u32 s44, s50, 0x1080
	s_addc_u32 s45, s51, 0
	v_cndmask_b32_e64 v132, v135, v157, s[42:43]
	v_cndmask_b32_e64 v161, v136, v159, s[42:43]
	v_lshl_add_u64 v[252:253], s[52:53], 0, v[136:137]
	v_lshl_add_u64 v[252:253], v[252:253], 0, s[20:21]
	global_load_lds_dwordx4 v[252:253], off
	v_lshl_add_u64 v[252:253], s[52:53], 0, v[138:139]
	v_lshl_add_u64 v[252:253], v[252:253], 0, s[20:21]
	s_mov_b32 m0, s29
	s_nop 0
	global_load_lds_dwordx4 v[252:253], off
	s_barrier
	s_waitcnt lgkmcnt(0)
	s_setprio 1
	v_mfma_f32_16x16x128_f8f6f4 v[116:119], v[218:225], v[178:185], v[116:119]
	v_mfma_f32_16x16x128_f8f6f4 v[112:115], v[226:233], v[178:185], v[112:115]
	v_mfma_f32_16x16x128_f8f6f4 v[100:103], v[218:225], v[186:193], v[100:103]
	v_mfma_f32_16x16x128_f8f6f4 v[96:99], v[226:233], v[186:193], v[96:99]
	v_mfma_f32_16x16x128_f8f6f4 v[84:87], v[218:225], v[196:203], v[84:87]
	v_mfma_f32_16x16x128_f8f6f4 v[80:83], v[226:233], v[196:203], v[80:83]
	v_mfma_f32_16x16x128_f8f6f4 v[68:71], v[218:225], v[204:211], v[68:71]
	v_mfma_f32_16x16x128_f8f6f4 v[64:67], v[226:233], v[204:211], v[64:67]
	s_setprio 0
	s_barrier
	s_mov_b32 m0, s0
	ds_read_b128 v[178:181], v145 offset:16384
	ds_read_b128 v[186:189], v145 offset:18432
	ds_read_b128 v[182:185], v146 offset:16384
	ds_read_b128 v[190:193], v146 offset:18432
	ds_read_b128 v[196:199], v145 offset:20480
	ds_read_b128 v[204:207], v145 offset:22528
	ds_read_b128 v[200:203], v146 offset:20480
	ds_read_b128 v[208:211], v146 offset:22528
	global_load_lds_dwordx4 v132, s[46:47]
	s_mov_b32 m0, s56
	v_mov_b32_e32 v141, v133
	global_load_lds_dwordx4 v140, s[46:47]
	s_barrier
	s_waitcnt lgkmcnt(0)
	v_lshl_add_u64 v[212:213], s[46:47], 0, v[132:133]
	v_lshl_add_u64 v[214:215], s[46:47], 0, v[140:141]
	s_setprio 1
	s_waitcnt lgkmcnt(0)
	v_mfma_f32_16x16x128_f8f6f4 v[60:63], v[162:169], v[178:185], v[60:63]
	v_mfma_f32_16x16x128_f8f6f4 v[56:59], v[170:177], v[178:185], v[56:59]
	v_mfma_f32_16x16x128_f8f6f4 v[44:47], v[162:169], v[186:193], v[44:47]
	v_mfma_f32_16x16x128_f8f6f4 v[40:43], v[170:177], v[186:193], v[40:43]
	v_mfma_f32_16x16x128_f8f6f4 v[28:31], v[162:169], v[196:203], v[28:31]
	v_mfma_f32_16x16x128_f8f6f4 v[24:27], v[170:177], v[196:203], v[24:27]
	v_mfma_f32_16x16x128_f8f6f4 v[12:15], v[162:169], v[204:211], v[12:15]
	v_mfma_f32_16x16x128_f8f6f4 v[8:11], v[170:177], v[204:211], v[8:11]
	s_setprio 0
	s_barrier
	s_mov_b32 m0, s1
	v_lshl_add_u64 v[140:141], s[50:51], 0, v[128:129]
	global_load_lds_dwordx4 v[140:141], off
	v_lshl_add_u64 v[142:143], s[50:51], 0, v[130:131]
	s_mov_b32 m0, s37
	s_nop 0
	global_load_lds_dwordx4 v[142:143], off
	s_waitcnt vmcnt(8)
	s_barrier
	s_setprio 1
	s_waitcnt lgkmcnt(0)
	v_mfma_f32_16x16x128_f8f6f4 v[52:55], v[218:225], v[178:185], v[52:55]
	v_mfma_f32_16x16x128_f8f6f4 v[48:51], v[226:233], v[178:185], v[48:51]
	v_mfma_f32_16x16x128_f8f6f4 v[36:39], v[218:225], v[186:193], v[36:39]
	v_mfma_f32_16x16x128_f8f6f4 v[32:35], v[226:233], v[186:193], v[32:35]
	v_mfma_f32_16x16x128_f8f6f4 v[20:23], v[218:225], v[196:203], v[20:23]
	v_mfma_f32_16x16x128_f8f6f4 v[16:19], v[226:233], v[196:203], v[16:19]
	v_mfma_f32_16x16x128_f8f6f4 v[4:7], v[218:225], v[204:211], v[4:7]
	v_mfma_f32_16x16x128_f8f6f4 v[0:3], v[226:233], v[204:211], v[0:3]
	s_setprio 0
	s_barrier
	ds_read_b128 v[162:165], v147 offset:32768
	ds_read_b128 v[170:173], v147 offset:34816
	ds_read_b128 v[166:169], v148 offset:32768
	ds_read_b128 v[174:177], v148 offset:34816
	s_mov_b32 m0, s65
	ds_read_b128 v[178:181], v145 offset:32768
	ds_read_b128 v[186:189], v145 offset:34816
	ds_read_b128 v[182:185], v146 offset:32768
	ds_read_b128 v[190:193], v146 offset:34816
	ds_read_b128 v[196:199], v145 offset:36864
	ds_read_b128 v[204:207], v145 offset:38912
	ds_read_b128 v[200:203], v146 offset:36864
	ds_read_b128 v[208:211], v146 offset:38912
	v_cndmask_b32_e64 v132, v138, v160, s[42:43]
	global_load_lds_dwordx4 v161, s[46:47]
	s_mov_b32 m0, s66
	s_nop 0
	global_load_lds_dwordx4 v132, s[46:47]
	s_waitcnt vmcnt(8)
	s_waitcnt lgkmcnt(8)
	s_barrier
	s_waitcnt lgkmcnt(0)
	s_setprio 1
	v_mfma_f32_16x16x128_f8f6f4 v[124:127], v[162:169], v[178:185], v[124:127]
	v_mfma_f32_16x16x128_f8f6f4 v[120:123], v[170:177], v[178:185], v[120:123]
	v_mfma_f32_16x16x128_f8f6f4 v[108:111], v[162:169], v[186:193], v[108:111]
	v_mfma_f32_16x16x128_f8f6f4 v[104:107], v[170:177], v[186:193], v[104:107]
	v_mfma_f32_16x16x128_f8f6f4 v[92:95], v[162:169], v[196:203], v[92:95]
	v_mfma_f32_16x16x128_f8f6f4 v[88:91], v[170:177], v[196:203], v[88:91]
	v_mfma_f32_16x16x128_f8f6f4 v[76:79], v[162:169], v[204:211], v[76:79]
	v_mfma_f32_16x16x128_f8f6f4 v[72:75], v[170:177], v[204:211], v[72:75]
	s_setprio 0
	s_barrier
	ds_read_b128 v[218:221], v147 offset:49152
	ds_read_b128 v[226:229], v147 offset:51200
	ds_read_b128 v[222:225], v148 offset:49152
	ds_read_b128 v[230:233], v148 offset:51200
	v_lshl_add_u64 v[216:217], s[48:49], 0, v[128:129]
	s_mov_b32 m0, s57
	s_nop 0
	global_load_lds_dwordx4 v[216:217], off
	v_lshl_add_u64 v[216:217], s[48:49], 0, v[130:131]
	s_mov_b32 m0, s64
	s_nop 0
	global_load_lds_dwordx4 v[216:217], off
	s_waitcnt vmcnt(8)
	s_barrier
	s_waitcnt lgkmcnt(0)
	s_setprio 1
	v_mfma_f32_16x16x128_f8f6f4 v[116:119], v[218:225], v[178:185], v[116:119]
	v_mfma_f32_16x16x128_f8f6f4 v[112:115], v[226:233], v[178:185], v[112:115]
	v_mfma_f32_16x16x128_f8f6f4 v[100:103], v[218:225], v[186:193], v[100:103]
	v_mfma_f32_16x16x128_f8f6f4 v[96:99], v[226:233], v[186:193], v[96:99]
	v_mfma_f32_16x16x128_f8f6f4 v[84:87], v[218:225], v[196:203], v[84:87]
	v_mfma_f32_16x16x128_f8f6f4 v[80:83], v[226:233], v[196:203], v[80:83]
	v_mfma_f32_16x16x128_f8f6f4 v[68:71], v[218:225], v[204:211], v[68:71]
	v_mfma_f32_16x16x128_f8f6f4 v[64:67], v[226:233], v[204:211], v[64:67]
	s_setprio 0
	s_barrier
	s_mov_b32 m0, s69
	v_lshl_add_u64 v[212:213], v[212:213], 0, s[20:21]
	ds_read_b128 v[178:181], v145 offset:49152
	ds_read_b128 v[186:189], v145 offset:51200
	ds_read_b128 v[182:185], v146 offset:49152
	ds_read_b128 v[190:193], v146 offset:51200
	ds_read_b128 v[196:199], v145 offset:53248
	ds_read_b128 v[204:207], v145 offset:55296
	ds_read_b128 v[200:203], v146 offset:53248
	ds_read_b128 v[208:211], v146 offset:55296
	global_load_lds_dwordx4 v[212:213], off
	v_lshl_add_u64 v[212:213], v[214:215], 0, s[20:21]
	s_mov_b32 m0, s70
	s_nop 0
	global_load_lds_dwordx4 v[212:213], off
	s_barrier
	s_waitcnt lgkmcnt(0)
	s_setprio 1
	v_mfma_f32_16x16x128_f8f6f4 v[60:63], v[162:169], v[178:185], v[60:63]
	v_mfma_f32_16x16x128_f8f6f4 v[56:59], v[170:177], v[178:185], v[56:59]
	v_mfma_f32_16x16x128_f8f6f4 v[44:47], v[162:169], v[186:193], v[44:47]
	v_mfma_f32_16x16x128_f8f6f4 v[40:43], v[170:177], v[186:193], v[40:43]
	v_mfma_f32_16x16x128_f8f6f4 v[28:31], v[162:169], v[196:203], v[28:31]
	v_mfma_f32_16x16x128_f8f6f4 v[24:27], v[170:177], v[196:203], v[24:27]
	v_mfma_f32_16x16x128_f8f6f4 v[12:15], v[162:169], v[204:211], v[12:15]
	v_mfma_f32_16x16x128_f8f6f4 v[8:11], v[170:177], v[204:211], v[8:11]
	s_setprio 0
	s_barrier
	s_mov_b32 m0, s67
	v_lshl_add_u64 v[140:141], v[140:141], 0, s[20:21]
	global_load_lds_dwordx4 v[140:141], off
	v_lshl_add_u64 v[140:141], v[142:143], 0, s[20:21]
	s_mov_b32 m0, s68
	s_nop 0
	global_load_lds_dwordx4 v[140:141], off
	s_waitcnt vmcnt(8)
	s_barrier
	s_setprio 1
	s_waitcnt lgkmcnt(0)
	v_mfma_f32_16x16x128_f8f6f4 v[52:55], v[218:225], v[178:185], v[52:55]
	v_mfma_f32_16x16x128_f8f6f4 v[48:51], v[226:233], v[178:185], v[48:51]
	v_mfma_f32_16x16x128_f8f6f4 v[36:39], v[218:225], v[186:193], v[36:39]
	v_mfma_f32_16x16x128_f8f6f4 v[32:35], v[226:233], v[186:193], v[32:35]
	v_mfma_f32_16x16x128_f8f6f4 v[20:23], v[218:225], v[196:203], v[20:23]
	v_mfma_f32_16x16x128_f8f6f4 v[16:19], v[226:233], v[196:203], v[16:19]
	v_mfma_f32_16x16x128_f8f6f4 v[4:7], v[218:225], v[204:211], v[4:7]
	v_mfma_f32_16x16x128_f8f6f4 v[0:3], v[226:233], v[204:211], v[0:3]
	s_setprio 0
	s_barrier
	s_mov_b32 m0, s71
	v_lshl_add_u64 v[140:141], s[44:45], 0, v[128:129]
	global_load_lds_dwordx4 v[140:141], off
	v_lshl_add_u64 v[140:141], s[44:45], 0, v[130:131]
	s_mov_b32 m0, s72
	s_andn2_b64 vcc, exec, s[40:41]
	global_load_lds_dwordx4 v[140:141], off
	s_mov_b64 s[42:43], -1
	s_mov_b64 s[40:41], 0
	s_mov_b64 s[44:45], 0x100
	s_cbranch_vccz .LBB0_1961

.LBB0_1988:
	v_mov_b32_e32 v137, v133
	v_mov_b32_e32 v139, v133
	s_mov_b64 s[34:35], 0
	s_mov_b64 s[28:29], -1
	s_mov_b64 s[30:31], 0
	s_add_u32 s42, s10, s34
	s_addc_u32 s43, s11, s35
	s_add_u32 s38, s42, 0x100
	s_addc_u32 s39, s43, 0
	s_and_b64 s[36:37], s[30:31], exec
	s_cselect_b32 s36, s10, s38
	s_cselect_b32 s37, s11, s39
	s_add_u32 s34, s26, s34
	s_addc_u32 s35, s27, s35
	s_add_u32 s38, s34, 0x100
	s_addc_u32 s39, s35, 0
	ds_read_b128 v[160:163], v147
	ds_read_b128 v[168:171], v147 offset:2048
	ds_read_b128 v[164:167], v148
	ds_read_b128 v[172:175], v148 offset:2048
	s_and_b64 s[34:35], s[30:31], exec
	s_cselect_b32 s41, s25, s39
	s_cselect_b32 s40, s24, s38
	ds_read_b128 v[176:179], v145
	ds_read_b128 v[184:187], v145 offset:2048
	ds_read_b128 v[180:183], v146
	ds_read_b128 v[188:191], v146 offset:2048
	ds_read_b128 v[196:199], v145 offset:4096
	ds_read_b128 v[204:207], v145 offset:6144
	ds_read_b128 v[200:203], v146 offset:4096
	ds_read_b128 v[208:211], v146 offset:6144
	s_waitcnt vmcnt(6)
	s_waitcnt lgkmcnt(8)
	s_barrier
	s_waitcnt lgkmcnt(0)
	v_cndmask_b32_e64 v140, v134, v156, s[30:31]
	s_setprio 1
	s_waitcnt lgkmcnt(0)
	v_mfma_f32_16x16x128_f8f6f4 v[124:127], v[160:167], v[176:183], 0
	v_mfma_f32_16x16x128_f8f6f4 v[120:123], v[168:175], v[176:183], 0
	v_mfma_f32_16x16x128_f8f6f4 v[108:111], v[160:167], v[184:191], 0
	v_mfma_f32_16x16x128_f8f6f4 v[104:107], v[168:175], v[184:191], 0
	v_mfma_f32_16x16x128_f8f6f4 v[92:95], v[160:167], v[196:203], 0
	v_mfma_f32_16x16x128_f8f6f4 v[88:91], v[168:175], v[196:203], 0
	v_mfma_f32_16x16x128_f8f6f4 v[76:79], v[160:167], v[204:211], 0
	v_mfma_f32_16x16x128_f8f6f4 v[72:75], v[168:175], v[204:211], 0
	s_setprio 0
	s_barrier
	ds_read_b128 v[218:221], v147 offset:16384
	ds_read_b128 v[226:229], v147 offset:18432
	ds_read_b128 v[222:225], v148 offset:16384
	ds_read_b128 v[230:233], v148 offset:18432
	s_add_i32 m0, s0, 0xc000
	s_add_i32 s62, s0, 0xe000
	s_add_u32 s38, s40, 0x1000
	s_addc_u32 s39, s41, 0
	s_add_u32 s34, s40, 0x1080
	s_addc_u32 s35, s41, 0
	v_cndmask_b32_e64 v132, v135, v155, s[30:31]
	v_cndmask_b32_e64 v159, v136, v157, s[30:31]
	v_lshl_add_u64 v[252:253], s[42:43], 0, v[136:137]
	v_lshl_add_u64 v[252:253], v[252:253], 0, s[16:17]
	global_load_lds_dwordx4 v[252:253], off
	v_lshl_add_u64 v[252:253], s[42:43], 0, v[138:139]
	v_lshl_add_u64 v[252:253], v[252:253], 0, s[16:17]
	s_mov_b32 m0, s62
	s_nop 0
	global_load_lds_dwordx4 v[252:253], off
	s_barrier
	s_waitcnt lgkmcnt(0)
	s_setprio 1
	v_mfma_f32_16x16x128_f8f6f4 v[116:119], v[218:225], v[176:183], 0
	v_mfma_f32_16x16x128_f8f6f4 v[112:115], v[226:233], v[176:183], 0
	v_mfma_f32_16x16x128_f8f6f4 v[100:103], v[218:225], v[184:191], 0
	v_mfma_f32_16x16x128_f8f6f4 v[96:99], v[226:233], v[184:191], 0
	v_mfma_f32_16x16x128_f8f6f4 v[84:87], v[218:225], v[196:203], 0
	v_mfma_f32_16x16x128_f8f6f4 v[80:83], v[226:233], v[196:203], 0
	v_mfma_f32_16x16x128_f8f6f4 v[68:71], v[218:225], v[204:211], 0
	v_mfma_f32_16x16x128_f8f6f4 v[64:67], v[226:233], v[204:211], 0
	s_setprio 0
	s_barrier
	s_mov_b32 m0, s0
	ds_read_b128 v[176:179], v145 offset:16384
	ds_read_b128 v[184:187], v145 offset:18432
	ds_read_b128 v[180:183], v146 offset:16384
	ds_read_b128 v[188:191], v146 offset:18432
	ds_read_b128 v[196:199], v145 offset:20480
	ds_read_b128 v[204:207], v145 offset:22528
	ds_read_b128 v[200:203], v146 offset:20480
	ds_read_b128 v[208:211], v146 offset:22528
	global_load_lds_dwordx4 v132, s[36:37]
	s_mov_b32 m0, s47
	v_mov_b32_e32 v141, v133
	global_load_lds_dwordx4 v140, s[36:37]
	s_barrier
	s_waitcnt lgkmcnt(0)
	v_lshl_add_u64 v[192:193], s[36:37], 0, v[132:133]
	v_lshl_add_u64 v[212:213], s[36:37], 0, v[140:141]
	s_setprio 1
	s_waitcnt lgkmcnt(0)
	v_mfma_f32_16x16x128_f8f6f4 v[60:63], v[160:167], v[176:183], 0
	v_mfma_f32_16x16x128_f8f6f4 v[56:59], v[168:175], v[176:183], 0
	v_mfma_f32_16x16x128_f8f6f4 v[44:47], v[160:167], v[184:191], 0
	v_mfma_f32_16x16x128_f8f6f4 v[40:43], v[168:175], v[184:191], 0
	v_mfma_f32_16x16x128_f8f6f4 v[28:31], v[160:167], v[196:203], 0
	v_mfma_f32_16x16x128_f8f6f4 v[24:27], v[168:175], v[196:203], 0
	v_mfma_f32_16x16x128_f8f6f4 v[12:15], v[160:167], v[204:211], 0
	v_mfma_f32_16x16x128_f8f6f4 v[8:11], v[168:175], v[204:211], 0
	s_setprio 0
	s_barrier
	s_mov_b32 m0, s1
	v_lshl_add_u64 v[140:141], s[40:41], 0, v[128:129]
	global_load_lds_dwordx4 v[140:141], off
	v_lshl_add_u64 v[142:143], s[40:41], 0, v[130:131]
	s_mov_b32 m0, s46
	s_nop 0
	global_load_lds_dwordx4 v[142:143], off
	s_waitcnt vmcnt(8)
	s_barrier
	s_setprio 1
	s_waitcnt lgkmcnt(0)
	v_mfma_f32_16x16x128_f8f6f4 v[52:55], v[218:225], v[176:183], 0
	v_mfma_f32_16x16x128_f8f6f4 v[48:51], v[226:233], v[176:183], 0
	v_mfma_f32_16x16x128_f8f6f4 v[36:39], v[218:225], v[184:191], 0
	v_mfma_f32_16x16x128_f8f6f4 v[32:35], v[226:233], v[184:191], 0
	v_mfma_f32_16x16x128_f8f6f4 v[20:23], v[218:225], v[196:203], 0
	v_mfma_f32_16x16x128_f8f6f4 v[16:19], v[226:233], v[196:203], 0
	v_mfma_f32_16x16x128_f8f6f4 v[4:7], v[218:225], v[204:211], 0
	v_mfma_f32_16x16x128_f8f6f4 v[0:3], v[226:233], v[204:211], 0
	s_setprio 0
	s_barrier
	ds_read_b128 v[160:163], v147 offset:32768
	ds_read_b128 v[168:171], v147 offset:34816
	ds_read_b128 v[164:167], v148 offset:32768
	ds_read_b128 v[172:175], v148 offset:34816
	s_mov_b32 m0, s50
	ds_read_b128 v[176:179], v145 offset:32768
	ds_read_b128 v[184:187], v145 offset:34816
	ds_read_b128 v[180:183], v146 offset:32768
	ds_read_b128 v[188:191], v146 offset:34816
	ds_read_b128 v[196:199], v145 offset:36864
	ds_read_b128 v[204:207], v145 offset:38912
	ds_read_b128 v[200:203], v146 offset:36864
	ds_read_b128 v[208:211], v146 offset:38912
	v_cndmask_b32_e64 v132, v138, v158, s[30:31]
	global_load_lds_dwordx4 v159, s[36:37]
	s_mov_b32 m0, s51
	s_nop 0
	global_load_lds_dwordx4 v132, s[36:37]
	s_waitcnt vmcnt(8)
	s_waitcnt lgkmcnt(8)
	s_barrier
	s_waitcnt lgkmcnt(0)
	s_setprio 1
	v_mfma_f32_16x16x128_f8f6f4 v[124:127], v[160:167], v[176:183], v[124:127]
	v_mfma_f32_16x16x128_f8f6f4 v[120:123], v[168:175], v[176:183], v[120:123]
	v_mfma_f32_16x16x128_f8f6f4 v[108:111], v[160:167], v[184:191], v[108:111]
	v_mfma_f32_16x16x128_f8f6f4 v[104:107], v[168:175], v[184:191], v[104:107]
	v_mfma_f32_16x16x128_f8f6f4 v[92:95], v[160:167], v[196:203], v[92:95]
	v_mfma_f32_16x16x128_f8f6f4 v[88:91], v[168:175], v[196:203], v[88:91]
	v_mfma_f32_16x16x128_f8f6f4 v[76:79], v[160:167], v[204:211], v[76:79]
	v_mfma_f32_16x16x128_f8f6f4 v[72:75], v[168:175], v[204:211], v[72:75]
	s_setprio 0
	s_barrier
	ds_read_b128 v[218:221], v147 offset:49152
	ds_read_b128 v[226:229], v147 offset:51200
	ds_read_b128 v[222:225], v148 offset:49152
	ds_read_b128 v[230:233], v148 offset:51200
	v_lshl_add_u64 v[214:215], s[38:39], 0, v[128:129]
	s_mov_b32 m0, s48
	s_nop 0
	global_load_lds_dwordx4 v[214:215], off
	v_lshl_add_u64 v[214:215], s[38:39], 0, v[130:131]
	s_mov_b32 m0, s49
	s_nop 0
	global_load_lds_dwordx4 v[214:215], off
	s_waitcnt vmcnt(8)
	s_barrier
	s_waitcnt lgkmcnt(0)
	s_setprio 1
	v_mfma_f32_16x16x128_f8f6f4 v[116:119], v[218:225], v[176:183], v[116:119]
	v_mfma_f32_16x16x128_f8f6f4 v[112:115], v[226:233], v[176:183], v[112:115]
	v_mfma_f32_16x16x128_f8f6f4 v[100:103], v[218:225], v[184:191], v[100:103]
	v_mfma_f32_16x16x128_f8f6f4 v[96:99], v[226:233], v[184:191], v[96:99]
	v_mfma_f32_16x16x128_f8f6f4 v[84:87], v[218:225], v[196:203], v[84:87]
	v_mfma_f32_16x16x128_f8f6f4 v[80:83], v[226:233], v[196:203], v[80:83]
	v_mfma_f32_16x16x128_f8f6f4 v[68:71], v[218:225], v[204:211], v[68:71]
	v_mfma_f32_16x16x128_f8f6f4 v[64:67], v[226:233], v[204:211], v[64:67]
	s_setprio 0
	s_barrier
	s_mov_b32 m0, s55
	v_lshl_add_u64 v[192:193], v[192:193], 0, s[16:17]
	ds_read_b128 v[176:179], v145 offset:49152
	ds_read_b128 v[184:187], v145 offset:51200
	ds_read_b128 v[180:183], v146 offset:49152
	ds_read_b128 v[188:191], v146 offset:51200
	ds_read_b128 v[196:199], v145 offset:53248
	ds_read_b128 v[204:207], v145 offset:55296
	ds_read_b128 v[200:203], v146 offset:53248
	ds_read_b128 v[208:211], v146 offset:55296
	global_load_lds_dwordx4 v[192:193], off
	v_lshl_add_u64 v[192:193], v[212:213], 0, s[16:17]
	s_mov_b32 m0, s56
	s_nop 0
	global_load_lds_dwordx4 v[192:193], off
	s_barrier
	s_waitcnt lgkmcnt(0)
	s_setprio 1
	v_mfma_f32_16x16x128_f8f6f4 v[60:63], v[160:167], v[176:183], v[60:63]
	v_mfma_f32_16x16x128_f8f6f4 v[56:59], v[168:175], v[176:183], v[56:59]
	v_mfma_f32_16x16x128_f8f6f4 v[44:47], v[160:167], v[184:191], v[44:47]
	v_mfma_f32_16x16x128_f8f6f4 v[40:43], v[168:175], v[184:191], v[40:43]
	v_mfma_f32_16x16x128_f8f6f4 v[28:31], v[160:167], v[196:203], v[28:31]
	v_mfma_f32_16x16x128_f8f6f4 v[24:27], v[168:175], v[196:203], v[24:27]
	v_mfma_f32_16x16x128_f8f6f4 v[12:15], v[160:167], v[204:211], v[12:15]
	v_mfma_f32_16x16x128_f8f6f4 v[8:11], v[168:175], v[204:211], v[8:11]
	s_setprio 0
	s_barrier
	s_mov_b32 m0, s53
	v_lshl_add_u64 v[140:141], v[140:141], 0, s[16:17]
	global_load_lds_dwordx4 v[140:141], off
	v_lshl_add_u64 v[140:141], v[142:143], 0, s[16:17]
	s_mov_b32 m0, s54
	s_nop 0
	global_load_lds_dwordx4 v[140:141], off
	s_waitcnt vmcnt(8)
	s_barrier
	s_setprio 1
	s_waitcnt lgkmcnt(0)
	v_mfma_f32_16x16x128_f8f6f4 v[52:55], v[218:225], v[176:183], v[52:55]
	v_mfma_f32_16x16x128_f8f6f4 v[48:51], v[226:233], v[176:183], v[48:51]
	v_mfma_f32_16x16x128_f8f6f4 v[36:39], v[218:225], v[184:191], v[36:39]
	v_mfma_f32_16x16x128_f8f6f4 v[32:35], v[226:233], v[184:191], v[32:35]
	v_mfma_f32_16x16x128_f8f6f4 v[20:23], v[218:225], v[196:203], v[20:23]
	v_mfma_f32_16x16x128_f8f6f4 v[16:19], v[226:233], v[196:203], v[16:19]
	v_mfma_f32_16x16x128_f8f6f4 v[4:7], v[218:225], v[204:211], v[4:7]
	v_mfma_f32_16x16x128_f8f6f4 v[0:3], v[226:233], v[204:211], v[0:3]
	s_setprio 0
	s_barrier
	s_mov_b32 m0, s57
	v_lshl_add_u64 v[140:141], s[34:35], 0, v[128:129]
	global_load_lds_dwordx4 v[140:141], off
	v_lshl_add_u64 v[140:141], s[34:35], 0, v[130:131]
	s_mov_b32 m0, s58
	s_andn2_b64 vcc, exec, s[28:29]
	global_load_lds_dwordx4 v[140:141], off
	s_mov_b64 s[30:31], -1
	s_mov_b64 s[28:29], 0
	s_mov_b64 s[34:35], 0x100
	s_cbranch_vccz .LBB0_1989
	s_branch .Lpeel_after_1989
.LBB0_1989:
	s_add_u32 s42, s10, s34
	s_addc_u32 s43, s11, s35
	s_add_u32 s38, s42, 0x100
	s_addc_u32 s39, s43, 0
	s_and_b64 s[36:37], s[30:31], exec
	s_cselect_b32 s36, s10, s38
	s_cselect_b32 s37, s11, s39
	s_add_u32 s34, s26, s34
	s_addc_u32 s35, s27, s35
	s_add_u32 s38, s34, 0x100
	s_addc_u32 s39, s35, 0
	ds_read_b128 v[160:163], v147
	ds_read_b128 v[168:171], v147 offset:2048
	ds_read_b128 v[164:167], v148
	ds_read_b128 v[172:175], v148 offset:2048
	s_and_b64 s[34:35], s[30:31], exec
	s_cselect_b32 s41, s25, s39
	s_cselect_b32 s40, s24, s38
	ds_read_b128 v[176:179], v145
	ds_read_b128 v[184:187], v145 offset:2048
	ds_read_b128 v[180:183], v146
	ds_read_b128 v[188:191], v146 offset:2048
	ds_read_b128 v[196:199], v145 offset:4096
	ds_read_b128 v[204:207], v145 offset:6144
	ds_read_b128 v[200:203], v146 offset:4096
	ds_read_b128 v[208:211], v146 offset:6144
	s_waitcnt vmcnt(6)
	s_waitcnt lgkmcnt(8)
	s_barrier
	s_waitcnt lgkmcnt(0)
	v_cndmask_b32_e64 v140, v134, v156, s[30:31]
	s_setprio 1
	s_waitcnt lgkmcnt(0)
	v_mfma_f32_16x16x128_f8f6f4 v[124:127], v[160:167], v[176:183], v[124:127]
	v_mfma_f32_16x16x128_f8f6f4 v[120:123], v[168:175], v[176:183], v[120:123]
	v_mfma_f32_16x16x128_f8f6f4 v[108:111], v[160:167], v[184:191], v[108:111]
	v_mfma_f32_16x16x128_f8f6f4 v[104:107], v[168:175], v[184:191], v[104:107]
	v_mfma_f32_16x16x128_f8f6f4 v[92:95], v[160:167], v[196:203], v[92:95]
	v_mfma_f32_16x16x128_f8f6f4 v[88:91], v[168:175], v[196:203], v[88:91]
	v_mfma_f32_16x16x128_f8f6f4 v[76:79], v[160:167], v[204:211], v[76:79]
	v_mfma_f32_16x16x128_f8f6f4 v[72:75], v[168:175], v[204:211], v[72:75]
	s_setprio 0
	s_barrier
	ds_read_b128 v[218:221], v147 offset:16384
	ds_read_b128 v[226:229], v147 offset:18432
	ds_read_b128 v[222:225], v148 offset:16384
	ds_read_b128 v[230:233], v148 offset:18432
	s_add_i32 m0, s0, 0xc000
	s_add_i32 s62, s0, 0xe000
	s_add_u32 s38, s40, 0x1000
	s_addc_u32 s39, s41, 0
	s_add_u32 s34, s40, 0x1080
	s_addc_u32 s35, s41, 0
	v_cndmask_b32_e64 v132, v135, v155, s[30:31]
	v_cndmask_b32_e64 v159, v136, v157, s[30:31]
	v_lshl_add_u64 v[252:253], s[42:43], 0, v[136:137]
	v_lshl_add_u64 v[252:253], v[252:253], 0, s[16:17]
	global_load_lds_dwordx4 v[252:253], off
	v_lshl_add_u64 v[252:253], s[42:43], 0, v[138:139]
	v_lshl_add_u64 v[252:253], v[252:253], 0, s[16:17]
	s_mov_b32 m0, s62
	s_nop 0
	global_load_lds_dwordx4 v[252:253], off
	s_barrier
	s_waitcnt lgkmcnt(0)
	s_setprio 1
	v_mfma_f32_16x16x128_f8f6f4 v[116:119], v[218:225], v[176:183], v[116:119]
	v_mfma_f32_16x16x128_f8f6f4 v[112:115], v[226:233], v[176:183], v[112:115]
	v_mfma_f32_16x16x128_f8f6f4 v[100:103], v[218:225], v[184:191], v[100:103]
	v_mfma_f32_16x16x128_f8f6f4 v[96:99], v[226:233], v[184:191], v[96:99]
	v_mfma_f32_16x16x128_f8f6f4 v[84:87], v[218:225], v[196:203], v[84:87]
	v_mfma_f32_16x16x128_f8f6f4 v[80:83], v[226:233], v[196:203], v[80:83]
	v_mfma_f32_16x16x128_f8f6f4 v[68:71], v[218:225], v[204:211], v[68:71]
	v_mfma_f32_16x16x128_f8f6f4 v[64:67], v[226:233], v[204:211], v[64:67]
	s_setprio 0
	s_barrier
	s_mov_b32 m0, s0
	ds_read_b128 v[176:179], v145 offset:16384
	ds_read_b128 v[184:187], v145 offset:18432
	ds_read_b128 v[180:183], v146 offset:16384
	ds_read_b128 v[188:191], v146 offset:18432
	ds_read_b128 v[196:199], v145 offset:20480
	ds_read_b128 v[204:207], v145 offset:22528
	ds_read_b128 v[200:203], v146 offset:20480
	ds_read_b128 v[208:211], v146 offset:22528
	global_load_lds_dwordx4 v132, s[36:37]
	s_mov_b32 m0, s47
	v_mov_b32_e32 v141, v133
	global_load_lds_dwordx4 v140, s[36:37]
	s_barrier
	s_waitcnt lgkmcnt(0)
	v_lshl_add_u64 v[192:193], s[36:37], 0, v[132:133]
	v_lshl_add_u64 v[212:213], s[36:37], 0, v[140:141]
	s_setprio 1
	s_waitcnt lgkmcnt(0)
	v_mfma_f32_16x16x128_f8f6f4 v[60:63], v[160:167], v[176:183], v[60:63]
	v_mfma_f32_16x16x128_f8f6f4 v[56:59], v[168:175], v[176:183], v[56:59]
	v_mfma_f32_16x16x128_f8f6f4 v[44:47], v[160:167], v[184:191], v[44:47]
	v_mfma_f32_16x16x128_f8f6f4 v[40:43], v[168:175], v[184:191], v[40:43]
	v_mfma_f32_16x16x128_f8f6f4 v[28:31], v[160:167], v[196:203], v[28:31]
	v_mfma_f32_16x16x128_f8f6f4 v[24:27], v[168:175], v[196:203], v[24:27]
	v_mfma_f32_16x16x128_f8f6f4 v[12:15], v[160:167], v[204:211], v[12:15]
	v_mfma_f32_16x16x128_f8f6f4 v[8:11], v[168:175], v[204:211], v[8:11]
	s_setprio 0
	s_barrier
	s_mov_b32 m0, s1
	v_lshl_add_u64 v[140:141], s[40:41], 0, v[128:129]
	global_load_lds_dwordx4 v[140:141], off
	v_lshl_add_u64 v[142:143], s[40:41], 0, v[130:131]
	s_mov_b32 m0, s46
	s_nop 0
	global_load_lds_dwordx4 v[142:143], off
	s_waitcnt vmcnt(8)
	s_barrier
	s_setprio 1
	s_waitcnt lgkmcnt(0)
	v_mfma_f32_16x16x128_f8f6f4 v[52:55], v[218:225], v[176:183], v[52:55]
	v_mfma_f32_16x16x128_f8f6f4 v[48:51], v[226:233], v[176:183], v[48:51]
	v_mfma_f32_16x16x128_f8f6f4 v[36:39], v[218:225], v[184:191], v[36:39]
	v_mfma_f32_16x16x128_f8f6f4 v[32:35], v[226:233], v[184:191], v[32:35]
	v_mfma_f32_16x16x128_f8f6f4 v[20:23], v[218:225], v[196:203], v[20:23]
	v_mfma_f32_16x16x128_f8f6f4 v[16:19], v[226:233], v[196:203], v[16:19]
	v_mfma_f32_16x16x128_f8f6f4 v[4:7], v[218:225], v[204:211], v[4:7]
	v_mfma_f32_16x16x128_f8f6f4 v[0:3], v[226:233], v[204:211], v[0:3]
	s_setprio 0
	s_barrier
	ds_read_b128 v[160:163], v147 offset:32768
	ds_read_b128 v[168:171], v147 offset:34816
	ds_read_b128 v[164:167], v148 offset:32768
	ds_read_b128 v[172:175], v148 offset:34816
	s_mov_b32 m0, s50
	ds_read_b128 v[176:179], v145 offset:32768
	ds_read_b128 v[184:187], v145 offset:34816
	ds_read_b128 v[180:183], v146 offset:32768
	ds_read_b128 v[188:191], v146 offset:34816
	ds_read_b128 v[196:199], v145 offset:36864
	ds_read_b128 v[204:207], v145 offset:38912
	ds_read_b128 v[200:203], v146 offset:36864
	ds_read_b128 v[208:211], v146 offset:38912
	v_cndmask_b32_e64 v132, v138, v158, s[30:31]
	global_load_lds_dwordx4 v159, s[36:37]
	s_mov_b32 m0, s51
	s_nop 0
	global_load_lds_dwordx4 v132, s[36:37]
	s_waitcnt vmcnt(8)
	s_waitcnt lgkmcnt(8)
	s_barrier
	s_waitcnt lgkmcnt(0)
	s_setprio 1
	v_mfma_f32_16x16x128_f8f6f4 v[124:127], v[160:167], v[176:183], v[124:127]
	v_mfma_f32_16x16x128_f8f6f4 v[120:123], v[168:175], v[176:183], v[120:123]
	v_mfma_f32_16x16x128_f8f6f4 v[108:111], v[160:167], v[184:191], v[108:111]
	v_mfma_f32_16x16x128_f8f6f4 v[104:107], v[168:175], v[184:191], v[104:107]
	v_mfma_f32_16x16x128_f8f6f4 v[92:95], v[160:167], v[196:203], v[92:95]
	v_mfma_f32_16x16x128_f8f6f4 v[88:91], v[168:175], v[196:203], v[88:91]
	v_mfma_f32_16x16x128_f8f6f4 v[76:79], v[160:167], v[204:211], v[76:79]
	v_mfma_f32_16x16x128_f8f6f4 v[72:75], v[168:175], v[204:211], v[72:75]
	s_setprio 0
	s_barrier
	ds_read_b128 v[218:221], v147 offset:49152
	ds_read_b128 v[226:229], v147 offset:51200
	ds_read_b128 v[222:225], v148 offset:49152
	ds_read_b128 v[230:233], v148 offset:51200
	v_lshl_add_u64 v[214:215], s[38:39], 0, v[128:129]
	s_mov_b32 m0, s48
	s_nop 0
	global_load_lds_dwordx4 v[214:215], off
	v_lshl_add_u64 v[214:215], s[38:39], 0, v[130:131]
	s_mov_b32 m0, s49
	s_nop 0
	global_load_lds_dwordx4 v[214:215], off
	s_waitcnt vmcnt(8)
	s_barrier
	s_waitcnt lgkmcnt(0)
	s_setprio 1
	v_mfma_f32_16x16x128_f8f6f4 v[116:119], v[218:225], v[176:183], v[116:119]
	v_mfma_f32_16x16x128_f8f6f4 v[112:115], v[226:233], v[176:183], v[112:115]
	v_mfma_f32_16x16x128_f8f6f4 v[100:103], v[218:225], v[184:191], v[100:103]
	v_mfma_f32_16x16x128_f8f6f4 v[96:99], v[226:233], v[184:191], v[96:99]
	v_mfma_f32_16x16x128_f8f6f4 v[84:87], v[218:225], v[196:203], v[84:87]
	v_mfma_f32_16x16x128_f8f6f4 v[80:83], v[226:233], v[196:203], v[80:83]
	v_mfma_f32_16x16x128_f8f6f4 v[68:71], v[218:225], v[204:211], v[68:71]
	v_mfma_f32_16x16x128_f8f6f4 v[64:67], v[226:233], v[204:211], v[64:67]
	s_setprio 0
	s_barrier
	s_mov_b32 m0, s55
	v_lshl_add_u64 v[192:193], v[192:193], 0, s[16:17]
	ds_read_b128 v[176:179], v145 offset:49152
	ds_read_b128 v[184:187], v145 offset:51200
	ds_read_b128 v[180:183], v146 offset:49152
	ds_read_b128 v[188:191], v146 offset:51200
	ds_read_b128 v[196:199], v145 offset:53248
	ds_read_b128 v[204:207], v145 offset:55296
	ds_read_b128 v[200:203], v146 offset:53248
	ds_read_b128 v[208:211], v146 offset:55296
	global_load_lds_dwordx4 v[192:193], off
	v_lshl_add_u64 v[192:193], v[212:213], 0, s[16:17]
	s_mov_b32 m0, s56
	s_nop 0
	global_load_lds_dwordx4 v[192:193], off
	s_barrier
	s_waitcnt lgkmcnt(0)
	s_setprio 1
	v_mfma_f32_16x16x128_f8f6f4 v[60:63], v[160:167], v[176:183], v[60:63]
	v_mfma_f32_16x16x128_f8f6f4 v[56:59], v[168:175], v[176:183], v[56:59]
	v_mfma_f32_16x16x128_f8f6f4 v[44:47], v[160:167], v[184:191], v[44:47]
	v_mfma_f32_16x16x128_f8f6f4 v[40:43], v[168:175], v[184:191], v[40:43]
	v_mfma_f32_16x16x128_f8f6f4 v[28:31], v[160:167], v[196:203], v[28:31]
	v_mfma_f32_16x16x128_f8f6f4 v[24:27], v[168:175], v[196:203], v[24:27]
	v_mfma_f32_16x16x128_f8f6f4 v[12:15], v[160:167], v[204:211], v[12:15]
	v_mfma_f32_16x16x128_f8f6f4 v[8:11], v[168:175], v[204:211], v[8:11]
	s_setprio 0
	s_barrier
	s_mov_b32 m0, s53
	v_lshl_add_u64 v[140:141], v[140:141], 0, s[16:17]
	global_load_lds_dwordx4 v[140:141], off
	v_lshl_add_u64 v[140:141], v[142:143], 0, s[16:17]
	s_mov_b32 m0, s54
	s_nop 0
	global_load_lds_dwordx4 v[140:141], off
	s_waitcnt vmcnt(8)
	s_barrier
	s_setprio 1
	s_waitcnt lgkmcnt(0)
	v_mfma_f32_16x16x128_f8f6f4 v[52:55], v[218:225], v[176:183], v[52:55]
	v_mfma_f32_16x16x128_f8f6f4 v[48:51], v[226:233], v[176:183], v[48:51]
	v_mfma_f32_16x16x128_f8f6f4 v[36:39], v[218:225], v[184:191], v[36:39]
	v_mfma_f32_16x16x128_f8f6f4 v[32:35], v[226:233], v[184:191], v[32:35]
	v_mfma_f32_16x16x128_f8f6f4 v[20:23], v[218:225], v[196:203], v[20:23]
	v_mfma_f32_16x16x128_f8f6f4 v[16:19], v[226:233], v[196:203], v[16:19]
	v_mfma_f32_16x16x128_f8f6f4 v[4:7], v[218:225], v[204:211], v[4:7]
	v_mfma_f32_16x16x128_f8f6f4 v[0:3], v[226:233], v[204:211], v[0:3]
	s_setprio 0
	s_barrier
	s_mov_b32 m0, s57
	v_lshl_add_u64 v[140:141], s[34:35], 0, v[128:129]
	global_load_lds_dwordx4 v[140:141], off
	v_lshl_add_u64 v[140:141], s[34:35], 0, v[130:131]
	s_mov_b32 m0, s58
	s_andn2_b64 vcc, exec, s[28:29]
	global_load_lds_dwordx4 v[140:141], off
	s_mov_b64 s[30:31], -1
	s_mov_b64 s[28:29], 0
	s_mov_b64 s[34:35], 0x100
	s_cbranch_vccz .LBB0_1989
